# v35 + P2a: skip the four dead W row-loads of the last half-step (tile 18) so the loop-exit vmcnt(0) no longer drains them
# speedup vs baseline: 1.0113x; 1.0113x over previous
.LBB0_267:
	s_waitcnt vmcnt(4)
	s_min_u32 s6, s50, 12
	ds_read_b128 v[148:151], v172
	ds_read_b128 v[152:155], v172 offset:2048
	ds_read_b128 v[156:159], v172 offset:4096
	ds_read_b64_tr_b16 v[178:179], v171
	ds_read_b64_tr_b16 v[180:181], v171 offset:1024
	s_cmp_lt_u32 s50, 13
	s_cselect_b64 vcc, -1, 0
	s_lshl_b32 s6, s6, 17
	s_add_u32 s51, s22, s6
	s_addc_u32 s77, s23, 0
	s_add_u32 s6, s51, 0x60000
	ds_read_b64_tr_b16 v[182:183], v141
	ds_read_b64_tr_b16 v[184:185], v141 offset:1024
	s_addc_u32 s7, s77, 0
	s_waitcnt lgkmcnt(2)
	v_mfma_f32_16x16x32_bf16 v[94:97], v[178:181], v[148:151], v[94:97]
	s_add_u32 s48, s18, s10
	s_addc_u32 s49, s19, s11
	s_add_u32 s48, s48, 0x80
	v_mfma_f32_16x16x32_bf16 v[74:77], v[178:181], v[152:155], v[74:77]
	v_cvt_pk_bf16_f32 v106, v106, v107
	v_cvt_pk_bf16_f32 v107, v108, v109
	v_cndmask_b32_e32 v160, 0, v168, vcc
	v_mfma_f32_16x16x32_bf16 v[78:81], v[178:181], v[156:159], v[78:81]
	s_addc_u32 s49, s49, 0
	ds_write_b64 v135, v[106:107] offset:16384
	ds_read_b64_tr_b16 v[106:107], v142
	ds_read_b64_tr_b16 v[108:109], v142 offset:1024
	s_waitcnt lgkmcnt(3)
	v_mfma_f32_16x16x32_bf16 v[90:93], v[182:185], v[148:151], v[90:93]
	v_cvt_pk_bf16_f32 v102, v102, v103
	v_cvt_pk_bf16_f32 v103, v104, v105
	ds_write_b64 v136, v[102:103] offset:16640
	v_mfma_f32_16x16x32_bf16 v[46:49], v[182:185], v[152:155], v[46:49]
	v_mfma_f32_16x16x32_bf16 v[58:61], v[182:185], v[156:159], v[58:61]
	ds_read_b64_tr_b16 v[102:103], v143
	ds_read_b64_tr_b16 v[104:105], v143 offset:1024
	s_waitcnt lgkmcnt(3)
	v_mfma_f32_16x16x32_bf16 v[70:73], v[106:109], v[148:151], v[70:73]
	v_cvt_pk_bf16_f32 v110, v110, v111
	v_cvt_pk_bf16_f32 v111, v112, v113
	ds_write_b64 v137, v[110:111] offset:16896
	v_mfma_f32_16x16x32_bf16 v[18:21], v[106:109], v[152:155], v[18:21]
	v_mfma_f32_16x16x32_bf16 v[38:41], v[106:109], v[156:159], v[38:41]
	ds_read_b64_tr_b16 v[106:107], v144
	ds_read_b64_tr_b16 v[108:109], v144 offset:1024
	s_waitcnt lgkmcnt(3)
	v_mfma_f32_16x16x32_bf16 v[42:45], v[102:105], v[148:151], v[42:45]
	v_cvt_pk_bf16_f32 v98, v98, v99
	v_cvt_pk_bf16_f32 v99, v100, v101
	ds_write_b64 v138, v[98:99] offset:17152
	v_mfma_f32_16x16x32_bf16 v[6:9], v[102:105], v[152:155], v[6:9]
	v_mfma_f32_16x16x32_bf16 v[22:25], v[102:105], v[156:159], v[22:25]
	ds_read_b64_tr_b16 v[98:99], v145
	ds_read_b64_tr_b16 v[100:101], v145 offset:1024
	s_waitcnt lgkmcnt(3)
	v_mfma_f32_16x16x32_bf16 v[86:89], v[106:109], v[148:151], v[86:89]
	s_mov_b32 s78, m0
	s_mov_b32 m0, s71
	s_nop 0
	global_load_lds_dwordx4 v169, s[48:49]
	s_mov_b32 m0, s78
	v_mfma_f32_16x16x32_bf16 v[54:57], v[106:109], v[152:155], v[54:57]
	v_mfma_f32_16x16x32_bf16 v[82:85], v[106:109], v[156:159], v[82:85]
	ds_read_b64_tr_b16 v[102:103], v146
	ds_read_b64_tr_b16 v[104:105], v146 offset:1024
	s_waitcnt lgkmcnt(2)
	v_mfma_f32_16x16x32_bf16 v[62:65], v[98:101], v[148:151], v[62:65]
	s_mov_b32 s78, m0
	s_mov_b32 m0, s72
	s_nop 0
	global_load_lds_dwordx4 v170, s[48:49]
	s_mov_b32 m0, s78
	v_mfma_f32_16x16x32_bf16 v[34:37], v[98:101], v[152:155], v[34:37]
	v_mfma_f32_16x16x32_bf16 v[66:69], v[98:101], v[156:159], v[66:69]
	ds_read_b64_tr_b16 v[98:99], v147
	ds_read_b64_tr_b16 v[100:101], v147 offset:1024
	s_waitcnt lgkmcnt(2)
	v_mfma_f32_16x16x32_bf16 v[30:33], v[102:105], v[148:151], v[30:33]
	s_mov_b32 s78, m0
	s_mov_b32 m0, s73
	s_nop 0
	global_load_lds_dwordx4 v174, s[48:49]
	s_mov_b32 m0, s78
	v_mfma_f32_16x16x32_bf16 v[14:17], v[102:105], v[152:155], v[14:17]
	v_mfma_f32_16x16x32_bf16 v[50:53], v[102:105], v[156:159], v[50:53]
	s_waitcnt lgkmcnt(0)
	v_mfma_f32_16x16x32_bf16 v[10:13], v[98:101], v[148:151], v[10:13]
	ds_read_b64_tr_b16 v[102:103], v171 offset:8192
	ds_read_b64_tr_b16 v[104:105], v171 offset:9216
	v_mfma_f32_16x16x32_bf16 v[2:5], v[98:101], v[152:155], v[2:5]
	ds_read_b128 v[148:151], v139
	ds_read_b128 v[152:155], v139 offset:2048
	ds_read_b128 v[178:181], v139 offset:4096
	s_mov_b32 s78, m0
	s_mov_b32 m0, s74
	s_nop 0
	global_load_lds_dwordx4 v175, s[48:49]
	s_mov_b32 m0, s78
	v_mfma_f32_16x16x32_bf16 v[26:29], v[98:101], v[156:159], v[26:29]
	ds_read_b64_tr_b16 v[98:99], v141 offset:8192
	ds_read_b64_tr_b16 v[100:101], v141 offset:9216
	s_waitcnt lgkmcnt(4)
	v_mfma_f32_16x16x32_bf16 v[94:97], v[102:105], v[148:151], v[94:97]
	s_mov_b32 s78, m0
	s_mov_b32 m0, s75
	s_nop 0
	global_load_lds_dwordx4 v176, s[48:49]
	s_mov_b32 m0, s78
	s_waitcnt lgkmcnt(3)
	v_mfma_f32_16x16x32_bf16 v[74:77], v[102:105], v[152:155], v[74:77]
	s_waitcnt lgkmcnt(2)
	v_mfma_f32_16x16x32_bf16 v[78:81], v[102:105], v[178:181], v[78:81]
	ds_read_b64_tr_b16 v[102:103], v142 offset:8192
	ds_read_b64_tr_b16 v[104:105], v142 offset:9216
	s_waitcnt lgkmcnt(2)
	v_mfma_f32_16x16x32_bf16 v[90:93], v[98:101], v[148:151], v[90:93]
	s_mov_b32 s78, m0
	s_mov_b32 m0, s76
	s_nop 0
	global_load_lds_dwordx4 v177, s[48:49]
	s_mov_b32 m0, s78
	v_mfma_f32_16x16x32_bf16 v[46:49], v[98:101], v[152:155], v[46:49]
	v_mfma_f32_16x16x32_bf16 v[58:61], v[98:101], v[178:181], v[58:61]
	ds_read_b64_tr_b16 v[98:99], v143 offset:8192
	ds_read_b64_tr_b16 v[100:101], v143 offset:9216
	s_waitcnt lgkmcnt(2)
	v_mfma_f32_16x16x32_bf16 v[70:73], v[102:105], v[148:151], v[70:73]
	v_mfma_f32_16x16x32_bf16 v[18:21], v[102:105], v[152:155], v[18:21]
	v_mfma_f32_16x16x32_bf16 v[38:41], v[102:105], v[178:181], v[38:41]
	ds_read_b64_tr_b16 v[102:103], v144 offset:8192
	ds_read_b64_tr_b16 v[104:105], v144 offset:9216
	s_waitcnt lgkmcnt(2)
	v_mfma_f32_16x16x32_bf16 v[42:45], v[98:101], v[148:151], v[42:45]
	v_mfma_f32_16x16x32_bf16 v[6:9], v[98:101], v[152:155], v[6:9]
	v_mfma_f32_16x16x32_bf16 v[22:25], v[98:101], v[178:181], v[22:25]
	ds_read_b64_tr_b16 v[98:99], v145 offset:8192
	ds_read_b64_tr_b16 v[100:101], v145 offset:9216
	s_waitcnt lgkmcnt(2)
	v_mfma_f32_16x16x32_bf16 v[86:89], v[102:105], v[148:151], v[86:89]
	global_load_dwordx4 v[106:109], v160, s[6:7]
	v_mfma_f32_16x16x32_bf16 v[54:57], v[102:105], v[152:155], v[54:57]
	v_mfma_f32_16x16x32_bf16 v[82:85], v[102:105], v[178:181], v[82:85]
	ds_read_b64_tr_b16 v[156:157], v146 offset:8192
	ds_read_b64_tr_b16 v[158:159], v146 offset:9216
	s_waitcnt lgkmcnt(2)
	v_mfma_f32_16x16x32_bf16 v[62:65], v[98:101], v[148:151], v[62:65]
	global_load_dwordx4 v[102:105], v160, s[6:7] offset:2048
	v_mfma_f32_16x16x32_bf16 v[34:37], v[98:101], v[152:155], v[34:37]
	v_mfma_f32_16x16x32_bf16 v[66:69], v[98:101], v[178:181], v[66:69]
	ds_read_b64_tr_b16 v[182:183], v147 offset:8192
	ds_read_b64_tr_b16 v[184:185], v147 offset:9216
	s_waitcnt lgkmcnt(2)
	v_mfma_f32_16x16x32_bf16 v[30:33], v[156:159], v[148:151], v[30:33]
	s_add_u32 s6, s51, 0x61000
	s_addc_u32 s7, s77, 0
	global_load_dwordx4 v[110:113], v160, s[6:7]
	v_mfma_f32_16x16x32_bf16 v[14:17], v[156:159], v[152:155], v[14:17]
	v_mfma_f32_16x16x32_bf16 v[50:53], v[156:159], v[178:181], v[50:53]
	s_waitcnt lgkmcnt(0)
	v_mfma_f32_16x16x32_bf16 v[10:13], v[182:185], v[148:151], v[10:13]
	global_load_dwordx4 v[98:101], v160, s[6:7] offset:2048
	v_mfma_f32_16x16x32_bf16 v[2:5], v[182:185], v[152:155], v[2:5]
	v_mfma_f32_16x16x32_bf16 v[26:29], v[182:185], v[178:181], v[26:29]
	s_min_u32 s6, s50, 11
	s_add_i32 s77, s50, 2
	s_cmp_lt_u32 s50, 12
	s_cselect_b64 vcc, -1, 0
	s_lshl_b32 s6, s6, 17
	s_waitcnt lgkmcnt(0)
	s_barrier
	s_add_u32 s78, s22, s6
	s_waitcnt vmcnt(4)
	s_addc_u32 s79, s23, 0
	s_add_u32 s48, s78, 0x80000
	ds_read_b64_tr_b16 v[148:149], v171 offset:16384
	ds_read_b64_tr_b16 v[150:151], v171 offset:17408
	ds_read_b128 v[152:155], v172 offset:8192
	ds_read_b128 v[156:159], v172 offset:10240
	ds_read_b128 v[178:181], v172 offset:12288
	s_addc_u32 s49, s79, 0
	s_add_u32 s10, s10, 0x100
	s_addc_u32 s11, s11, 0
	s_cmp_lt_u32 s50, 14
	ds_read_b64_tr_b16 v[182:183], v141 offset:16384
	ds_read_b64_tr_b16 v[184:185], v141 offset:17408
	s_cselect_b64 s[6:7], -1, 0
	s_waitcnt lgkmcnt(4)
	v_mfma_f32_16x16x32_bf16 v[94:97], v[148:151], v[152:155], v[94:97]
	v_cndmask_b32_e32 v160, 0, v168, vcc
	s_and_b64 vcc, s[6:7], exec
	s_cselect_b32 s50, s10, 0x780
	s_waitcnt lgkmcnt(3)
	v_mfma_f32_16x16x32_bf16 v[74:77], v[148:151], v[156:159], v[74:77]
	s_add_u32 s50, s18, s50
	v_cvt_pk_bf16_f32 v122, v122, v123
	v_cvt_pk_bf16_f32 v123, v124, v125
	s_waitcnt lgkmcnt(2)
	v_mfma_f32_16x16x32_bf16 v[78:81], v[148:151], v[178:181], v[78:81]
	s_addc_u32 s51, s19, 0
	ds_write_b64 v135, v[122:123]
	ds_read_b64_tr_b16 v[122:123], v142 offset:16384
	ds_read_b64_tr_b16 v[124:125], v142 offset:17408
	s_waitcnt lgkmcnt(3)
	v_mfma_f32_16x16x32_bf16 v[90:93], v[182:185], v[152:155], v[90:93]
	v_cvt_pk_bf16_f32 v118, v118, v119
	v_cvt_pk_bf16_f32 v119, v120, v121
	ds_write_b64 v136, v[118:119] offset:256
	v_mfma_f32_16x16x32_bf16 v[46:49], v[182:185], v[156:159], v[46:49]
	v_mfma_f32_16x16x32_bf16 v[58:61], v[182:185], v[178:181], v[58:61]
	ds_read_b64_tr_b16 v[118:119], v143 offset:16384
	ds_read_b64_tr_b16 v[120:121], v143 offset:17408
	s_waitcnt lgkmcnt(3)
	v_mfma_f32_16x16x32_bf16 v[70:73], v[122:125], v[152:155], v[70:73]
	v_cvt_pk_bf16_f32 v126, v126, v127
	v_cvt_pk_bf16_f32 v127, v128, v129
	ds_write_b64 v137, v[126:127] offset:512
	v_mfma_f32_16x16x32_bf16 v[18:21], v[122:125], v[156:159], v[18:21]
	v_mfma_f32_16x16x32_bf16 v[38:41], v[122:125], v[178:181], v[38:41]
	ds_read_b64_tr_b16 v[122:123], v144 offset:16384
	ds_read_b64_tr_b16 v[124:125], v144 offset:17408
	s_waitcnt lgkmcnt(3)
	v_mfma_f32_16x16x32_bf16 v[42:45], v[118:121], v[152:155], v[42:45]
	v_cvt_pk_bf16_f32 v114, v114, v115
	v_cvt_pk_bf16_f32 v115, v116, v117
	ds_write_b64 v138, v[114:115] offset:768
	v_mfma_f32_16x16x32_bf16 v[6:9], v[118:121], v[156:159], v[6:9]
	v_mfma_f32_16x16x32_bf16 v[22:25], v[118:121], v[178:181], v[22:25]
	ds_read_b64_tr_b16 v[114:115], v145 offset:16384
	ds_read_b64_tr_b16 v[116:117], v145 offset:17408
	s_waitcnt lgkmcnt(3)
	v_mfma_f32_16x16x32_bf16 v[86:89], v[122:125], v[152:155], v[86:89]
	v_cndmask_b32_e64 v118, 0, v169, s[6:7]
	s_mov_b32 s80, m0
	s_mov_b32 m0, s67
	s_nop 0
	global_load_lds_dwordx4 v118, s[50:51]
	s_mov_b32 m0, s80
	v_mfma_f32_16x16x32_bf16 v[54:57], v[122:125], v[156:159], v[54:57]
	v_mfma_f32_16x16x32_bf16 v[82:85], v[122:125], v[178:181], v[82:85]
	ds_read_b64_tr_b16 v[118:119], v146 offset:16384
	ds_read_b64_tr_b16 v[120:121], v146 offset:17408
	s_waitcnt lgkmcnt(2)
	v_mfma_f32_16x16x32_bf16 v[62:65], v[114:117], v[152:155], v[62:65]
	v_cndmask_b32_e64 v122, 0, v170, s[6:7]
	s_mov_b32 s80, m0
	s_mov_b32 m0, s68
	s_nop 0
	global_load_lds_dwordx4 v122, s[50:51]
	s_mov_b32 m0, s80
	v_mfma_f32_16x16x32_bf16 v[34:37], v[114:117], v[156:159], v[34:37]
	v_mfma_f32_16x16x32_bf16 v[66:69], v[114:117], v[178:181], v[66:69]
	ds_read_b64_tr_b16 v[114:115], v147 offset:16384
	ds_read_b64_tr_b16 v[116:117], v147 offset:17408
	s_waitcnt lgkmcnt(2)
	v_mfma_f32_16x16x32_bf16 v[30:33], v[118:121], v[152:155], v[30:33]
	v_cndmask_b32_e64 v122, 0, v174, s[6:7]
	s_mov_b32 s80, m0
	s_mov_b32 m0, s52
	s_nop 0
	global_load_lds_dwordx4 v122, s[50:51]
	s_mov_b32 m0, s80
	v_mfma_f32_16x16x32_bf16 v[14:17], v[118:121], v[156:159], v[14:17]
	v_mfma_f32_16x16x32_bf16 v[50:53], v[118:121], v[178:181], v[50:53]
	s_waitcnt lgkmcnt(0)
	v_mfma_f32_16x16x32_bf16 v[10:13], v[114:117], v[152:155], v[10:13]
	ds_read_b64_tr_b16 v[118:119], v171 offset:24576
	ds_read_b64_tr_b16 v[120:121], v171 offset:25600
	v_cndmask_b32_e64 v122, 0, v175, s[6:7]
	v_mfma_f32_16x16x32_bf16 v[2:5], v[114:117], v[156:159], v[2:5]
	ds_read_b128 v[148:151], v140
	ds_read_b128 v[152:155], v140 offset:2048
	ds_read_b128 v[156:159], v140 offset:4096
	s_mov_b32 s80, m0
	s_mov_b32 m0, s53
	s_nop 0
	global_load_lds_dwordx4 v122, s[50:51]
	s_mov_b32 m0, s80
	v_mfma_f32_16x16x32_bf16 v[26:29], v[114:117], v[178:181], v[26:29]
	ds_read_b64_tr_b16 v[114:115], v141 offset:24576
	ds_read_b64_tr_b16 v[116:117], v141 offset:25600
	s_waitcnt lgkmcnt(4)
	v_mfma_f32_16x16x32_bf16 v[94:97], v[118:121], v[148:151], v[94:97]
	v_cndmask_b32_e64 v122, 0, v176, s[6:7]
	s_mov_b32 s80, m0
	s_mov_b32 m0, s69
	s_nop 0
	global_load_lds_dwordx4 v122, s[50:51]
	s_mov_b32 m0, s80
	s_waitcnt lgkmcnt(3)
	v_mfma_f32_16x16x32_bf16 v[74:77], v[118:121], v[152:155], v[74:77]
	s_waitcnt lgkmcnt(2)
	v_mfma_f32_16x16x32_bf16 v[78:81], v[118:121], v[156:159], v[78:81]
	ds_read_b64_tr_b16 v[118:119], v142 offset:24576
	ds_read_b64_tr_b16 v[120:121], v142 offset:25600
	s_waitcnt lgkmcnt(2)
	v_mfma_f32_16x16x32_bf16 v[90:93], v[114:117], v[148:151], v[90:93]
	v_cndmask_b32_e64 v122, 0, v177, s[6:7]
	s_mov_b32 s6, m0
	s_mov_b32 m0, s70
	s_nop 0
	global_load_lds_dwordx4 v122, s[50:51]
	s_mov_b32 m0, s6
	v_mfma_f32_16x16x32_bf16 v[46:49], v[114:117], v[152:155], v[46:49]
	v_mfma_f32_16x16x32_bf16 v[58:61], v[114:117], v[156:159], v[58:61]
	ds_read_b64_tr_b16 v[114:115], v143 offset:24576
	ds_read_b64_tr_b16 v[116:117], v143 offset:25600
	s_waitcnt lgkmcnt(2)
	v_mfma_f32_16x16x32_bf16 v[70:73], v[118:121], v[148:151], v[70:73]
	v_mfma_f32_16x16x32_bf16 v[18:21], v[118:121], v[152:155], v[18:21]
	v_mfma_f32_16x16x32_bf16 v[38:41], v[118:121], v[156:159], v[38:41]
	ds_read_b64_tr_b16 v[118:119], v144 offset:24576
	ds_read_b64_tr_b16 v[120:121], v144 offset:25600
	s_waitcnt lgkmcnt(2)
	v_mfma_f32_16x16x32_bf16 v[42:45], v[114:117], v[148:151], v[42:45]
	v_mfma_f32_16x16x32_bf16 v[6:9], v[114:117], v[152:155], v[6:9]
	v_mfma_f32_16x16x32_bf16 v[22:25], v[114:117], v[156:159], v[22:25]
	ds_read_b64_tr_b16 v[114:115], v145 offset:24576
	ds_read_b64_tr_b16 v[116:117], v145 offset:25600
	s_waitcnt lgkmcnt(2)
	v_mfma_f32_16x16x32_bf16 v[86:89], v[118:121], v[148:151], v[86:89]
	s_cbranch_vccz .Lmy_tl_267_0
	global_load_dwordx4 v[122:125], v160, s[48:49]
.Lmy_tl_267_0:
	v_mfma_f32_16x16x32_bf16 v[54:57], v[118:121], v[152:155], v[54:57]
	v_mfma_f32_16x16x32_bf16 v[82:85], v[118:121], v[156:159], v[82:85]
	ds_read_b64_tr_b16 v[178:179], v146 offset:24576
	ds_read_b64_tr_b16 v[180:181], v146 offset:25600
	s_waitcnt lgkmcnt(2)
	v_mfma_f32_16x16x32_bf16 v[62:65], v[114:117], v[148:151], v[62:65]
	s_cbranch_vccz .Lmy_tl_267_1
	global_load_dwordx4 v[118:121], v160, s[48:49] offset:2048
.Lmy_tl_267_1:
	v_mfma_f32_16x16x32_bf16 v[34:37], v[114:117], v[152:155], v[34:37]
	v_mfma_f32_16x16x32_bf16 v[66:69], v[114:117], v[156:159], v[66:69]
	ds_read_b64_tr_b16 v[182:183], v147 offset:24576
	ds_read_b64_tr_b16 v[184:185], v147 offset:25600
	s_waitcnt lgkmcnt(2)
	v_mfma_f32_16x16x32_bf16 v[30:33], v[178:181], v[148:151], v[30:33]
	s_add_u32 s6, s78, 0x81000
	s_addc_u32 s7, s79, 0
	s_cbranch_vccz .Lmy_tl_267_2
	global_load_dwordx4 v[126:129], v160, s[6:7]
.Lmy_tl_267_2:
	v_mfma_f32_16x16x32_bf16 v[14:17], v[178:181], v[152:155], v[14:17]
	v_mfma_f32_16x16x32_bf16 v[50:53], v[178:181], v[156:159], v[50:53]
	s_waitcnt lgkmcnt(0)
	v_mfma_f32_16x16x32_bf16 v[10:13], v[182:185], v[148:151], v[10:13]
	s_cbranch_vccz .Lmy_tl_267_3
	global_load_dwordx4 v[114:117], v160, s[6:7] offset:2048
.Lmy_tl_267_3:
	v_mfma_f32_16x16x32_bf16 v[2:5], v[182:185], v[152:155], v[2:5]
	v_mfma_f32_16x16x32_bf16 v[26:29], v[182:185], v[156:159], v[26:29]
	s_waitcnt lgkmcnt(0)
	s_barrier
	s_mov_b32 s50, s77
	s_cbranch_vccnz .LBB0_267
	s_waitcnt vmcnt(0)
	s_waitcnt lgkmcnt(0)
	s_barrier
	s_mov_b64 s[10:11], 0
	s_branch .LBB0_274

.LBB0_272:
	s_waitcnt vmcnt(4)
	s_min_u32 s6, s52, 12
	ds_read_b128 v[112:115], v172
	ds_read_b128 v[116:119], v172 offset:2048
	s_cmp_lt_u32 s52, 13
	ds_read_b64_tr_b16 v[120:121], v171
	ds_read_b64_tr_b16 v[122:123], v171 offset:1024
	s_cselect_b64 vcc, -1, 0
	s_lshl_b32 s6, s6, 17
	s_add_u32 s53, s22, s6
	s_addc_u32 s75, s23, 0
	s_add_u32 s6, s53, 0x60000
	ds_read_b64_tr_b16 v[124:125], v104
	ds_read_b64_tr_b16 v[126:127], v104 offset:1024
	s_addc_u32 s7, s75, 0
	s_waitcnt lgkmcnt(2)
	v_mfma_f32_16x16x32_bf16 v[94:97], v[120:123], v[112:115], v[94:97]
	s_add_u32 s50, s18, s48
	s_addc_u32 s51, s19, s49
	s_add_u32 s50, s50, 0x80
	v_mfma_f32_16x16x32_bf16 v[74:77], v[120:123], v[116:119], v[74:77]
	v_cvt_pk_bf16_f32 v38, v38, v39
	v_cvt_pk_bf16_f32 v39, v40, v41
	v_cndmask_b32_e32 v111, 0, v168, vcc
	s_addc_u32 s51, s51, 0
	ds_write_b64 v98, v[38:39] offset:16384
	ds_read_b64_tr_b16 v[38:39], v105
	ds_read_b64_tr_b16 v[40:41], v105 offset:1024
	v_cvt_pk_bf16_f32 v26, v26, v27
	v_cvt_pk_bf16_f32 v27, v28, v29
	s_waitcnt lgkmcnt(3)
	v_mfma_f32_16x16x32_bf16 v[90:93], v[124:127], v[112:115], v[90:93]
	ds_write_b64 v99, v[26:27] offset:16640
	v_mfma_f32_16x16x32_bf16 v[26:29], v[124:127], v[116:119], v[46:49]
	s_nop 2
	ds_read_b64_tr_b16 v[46:47], v106
	ds_read_b64_tr_b16 v[48:49], v106 offset:1024
	s_waitcnt lgkmcnt(3)
	v_mfma_f32_16x16x32_bf16 v[70:73], v[38:41], v[112:115], v[70:73]
	v_cvt_pk_bf16_f32 v50, v50, v51
	v_cvt_pk_bf16_f32 v51, v52, v53
	ds_write_b64 v100, v[50:51] offset:16896
	v_mfma_f32_16x16x32_bf16 v[18:21], v[38:41], v[116:119], v[18:21]
	ds_read_b64_tr_b16 v[38:39], v107
	ds_read_b64_tr_b16 v[40:41], v107 offset:1024
	s_waitcnt lgkmcnt(3)
	v_mfma_f32_16x16x32_bf16 v[42:45], v[46:49], v[112:115], v[42:45]
	v_cvt_pk_bf16_f32 v22, v22, v23
	v_cvt_pk_bf16_f32 v23, v24, v25
	ds_write_b64 v101, v[22:23] offset:17152
	v_mfma_f32_16x16x32_bf16 v[6:9], v[46:49], v[116:119], v[6:9]
	ds_read_b64_tr_b16 v[46:47], v108
	ds_read_b64_tr_b16 v[48:49], v108 offset:1024
	s_waitcnt lgkmcnt(3)
	v_mfma_f32_16x16x32_bf16 v[22:25], v[38:41], v[112:115], v[86:89]
	s_mov_b32 s76, m0
	s_mov_b32 m0, s71
	s_nop 0
	global_load_lds_dwordx4 v169, s[50:51]
	s_mov_b32 m0, s76
	v_mfma_f32_16x16x32_bf16 v[50:53], v[38:41], v[116:119], v[54:57]
	ds_read_b64_tr_b16 v[38:39], v109
	ds_read_b64_tr_b16 v[40:41], v109 offset:1024
	s_waitcnt lgkmcnt(2)
	v_mfma_f32_16x16x32_bf16 v[54:57], v[46:49], v[112:115], v[62:65]
	s_mov_b32 s76, m0
	s_mov_b32 m0, s72
	s_nop 0
	global_load_lds_dwordx4 v170, s[50:51]
	s_mov_b32 m0, s76
	v_mfma_f32_16x16x32_bf16 v[34:37], v[46:49], v[116:119], v[34:37]
	ds_read_b64_tr_b16 v[46:47], v110
	ds_read_b64_tr_b16 v[48:49], v110 offset:1024
	s_waitcnt lgkmcnt(2)
	v_mfma_f32_16x16x32_bf16 v[30:33], v[38:41], v[112:115], v[30:33]
	s_mov_b32 s76, m0
	s_mov_b32 m0, s73
	s_nop 0
	global_load_lds_dwordx4 v174, s[50:51]
	s_mov_b32 m0, s76
	v_mfma_f32_16x16x32_bf16 v[14:17], v[38:41], v[116:119], v[14:17]
	ds_read_b64_tr_b16 v[38:39], v171 offset:8192
	ds_read_b64_tr_b16 v[40:41], v171 offset:9216
	ds_read_b128 v[62:65], v102
	ds_read_b128 v[86:89], v102 offset:2048
	s_waitcnt lgkmcnt(4)
	v_mfma_f32_16x16x32_bf16 v[10:13], v[46:49], v[112:115], v[10:13]
	s_mov_b32 s76, m0
	s_mov_b32 m0, s74
	s_nop 0
	global_load_lds_dwordx4 v175, s[50:51]
	s_mov_b32 m0, s76
	v_mfma_f32_16x16x32_bf16 v[2:5], v[46:49], v[116:119], v[2:5]
	s_waitcnt lgkmcnt(1)
	v_mfma_f32_16x16x32_bf16 v[46:49], v[38:41], v[62:65], v[94:97]
	s_nop 2
	ds_read_b64_tr_b16 v[94:95], v104 offset:8192
	ds_read_b64_tr_b16 v[96:97], v104 offset:9216
	s_waitcnt lgkmcnt(2)
	v_mfma_f32_16x16x32_bf16 v[74:77], v[38:41], v[86:89], v[74:77]
	ds_read_b64_tr_b16 v[38:39], v105 offset:8192
	ds_read_b64_tr_b16 v[40:41], v105 offset:9216
	s_waitcnt lgkmcnt(2)
	v_mfma_f32_16x16x32_bf16 v[90:93], v[94:97], v[62:65], v[90:93]
	v_mfma_f32_16x16x32_bf16 v[94:97], v[94:97], v[86:89], v[26:29]
	s_nop 2
	ds_read_b64_tr_b16 v[26:27], v106 offset:8192
	ds_read_b64_tr_b16 v[28:29], v106 offset:9216
	s_waitcnt lgkmcnt(2)
	v_mfma_f32_16x16x32_bf16 v[70:73], v[38:41], v[62:65], v[70:73]
	v_mfma_f32_16x16x32_bf16 v[18:21], v[38:41], v[86:89], v[18:21]
	ds_read_b64_tr_b16 v[112:113], v107 offset:8192
	ds_read_b64_tr_b16 v[114:115], v107 offset:9216
	s_waitcnt lgkmcnt(2)
	v_mfma_f32_16x16x32_bf16 v[42:45], v[26:29], v[62:65], v[42:45]
	v_mfma_f32_16x16x32_bf16 v[6:9], v[26:29], v[86:89], v[6:9]
	s_waitcnt lgkmcnt(0)
	v_mfma_f32_16x16x32_bf16 v[116:119], v[112:115], v[62:65], v[22:25]
	s_nop 2
	ds_read_b64_tr_b16 v[22:23], v108 offset:8192
	ds_read_b64_tr_b16 v[24:25], v108 offset:9216
	global_load_dwordx4 v[38:41], v111, s[6:7]
	v_mfma_f32_16x16x32_bf16 v[112:115], v[112:115], v[86:89], v[50:53]
	ds_read_b64_tr_b16 v[120:121], v109 offset:8192
	ds_read_b64_tr_b16 v[122:123], v109 offset:9216
	s_waitcnt lgkmcnt(2)
	v_mfma_f32_16x16x32_bf16 v[54:57], v[22:25], v[62:65], v[54:57]
	global_load_dwordx4 v[26:29], v111, s[6:7] offset:2048
	v_mfma_f32_16x16x32_bf16 v[34:37], v[22:25], v[86:89], v[34:37]
	ds_read_b64_tr_b16 v[124:125], v110 offset:8192
	ds_read_b64_tr_b16 v[126:127], v110 offset:9216
	s_waitcnt lgkmcnt(2)
	v_mfma_f32_16x16x32_bf16 v[30:33], v[120:123], v[62:65], v[30:33]
	s_add_u32 s6, s53, 0x61000
	s_addc_u32 s7, s75, 0
	global_load_dwordx4 v[50:53], v111, s[6:7]
	v_mfma_f32_16x16x32_bf16 v[14:17], v[120:123], v[86:89], v[14:17]
	s_waitcnt lgkmcnt(0)
	v_mfma_f32_16x16x32_bf16 v[10:13], v[124:127], v[62:65], v[10:13]
	global_load_dwordx4 v[22:25], v111, s[6:7] offset:2048
	v_mfma_f32_16x16x32_bf16 v[2:5], v[124:127], v[86:89], v[2:5]
	s_min_u32 s6, s52, 11
	s_add_i32 s75, s52, 2
	s_cmp_lt_u32 s52, 12
	s_cselect_b64 vcc, -1, 0
	s_lshl_b32 s6, s6, 17
	s_waitcnt lgkmcnt(0)
	s_barrier
	s_add_u32 s76, s22, s6
	s_waitcnt vmcnt(4)
	s_addc_u32 s77, s23, 0
	s_add_u32 s50, s76, 0x80000
	ds_read_b64_tr_b16 v[62:63], v171 offset:16384
	ds_read_b64_tr_b16 v[64:65], v171 offset:17408
	ds_read_b128 v[86:89], v172 offset:8192
	ds_read_b128 v[120:123], v172 offset:10240
	s_addc_u32 s51, s77, 0
	s_add_u32 s48, s48, 0x100
	s_addc_u32 s49, s49, 0
	s_cmp_lt_u32 s52, 14
	ds_read_b64_tr_b16 v[124:125], v104 offset:16384
	ds_read_b64_tr_b16 v[126:127], v104 offset:17408
	s_cselect_b64 s[6:7], -1, 0
	s_waitcnt lgkmcnt(3)
	v_mfma_f32_16x16x32_bf16 v[46:49], v[62:65], v[86:89], v[46:49]
	v_cndmask_b32_e32 v111, 0, v168, vcc
	s_and_b64 vcc, s[6:7], exec
	s_cselect_b32 s52, s48, 0x780
	s_waitcnt lgkmcnt(2)
	v_mfma_f32_16x16x32_bf16 v[62:65], v[62:65], v[120:123], v[74:77]
	s_add_u32 s52, s18, s52
	s_addc_u32 s53, s19, 0
	s_nop 0
	v_cvt_pk_bf16_f32 v74, v78, v79
	v_cvt_pk_bf16_f32 v75, v80, v81
	ds_write_b64 v98, v[74:75]
	ds_read_b64_tr_b16 v[74:75], v105 offset:16384
	ds_read_b64_tr_b16 v[76:77], v105 offset:17408
	v_cvt_pk_bf16_f32 v66, v66, v67
	v_cvt_pk_bf16_f32 v67, v68, v69
	s_waitcnt lgkmcnt(3)
	v_mfma_f32_16x16x32_bf16 v[78:81], v[124:127], v[86:89], v[90:93]
	ds_write_b64 v99, v[66:67] offset:256
	v_mfma_f32_16x16x32_bf16 v[66:69], v[124:127], v[120:123], v[94:97]
	s_nop 0
	ds_read_b64_tr_b16 v[90:91], v106 offset:16384
	ds_read_b64_tr_b16 v[92:93], v106 offset:17408
	s_waitcnt lgkmcnt(3)
	v_mfma_f32_16x16x32_bf16 v[70:73], v[74:77], v[86:89], v[70:73]
	v_cvt_pk_bf16_f32 v82, v82, v83
	v_cvt_pk_bf16_f32 v83, v84, v85
	ds_write_b64 v100, v[82:83] offset:512
	v_mfma_f32_16x16x32_bf16 v[18:21], v[74:77], v[120:123], v[18:21]
	ds_read_b64_tr_b16 v[74:75], v107 offset:16384
	ds_read_b64_tr_b16 v[76:77], v107 offset:17408
	s_waitcnt lgkmcnt(3)
	v_mfma_f32_16x16x32_bf16 v[42:45], v[90:93], v[86:89], v[42:45]
	v_cvt_pk_bf16_f32 v58, v58, v59
	v_cvt_pk_bf16_f32 v59, v60, v61
	ds_write_b64 v101, v[58:59] offset:768
	v_mfma_f32_16x16x32_bf16 v[6:9], v[90:93], v[120:123], v[6:9]
	ds_read_b64_tr_b16 v[82:83], v108 offset:16384
	ds_read_b64_tr_b16 v[84:85], v108 offset:17408
	s_waitcnt lgkmcnt(3)
	v_mfma_f32_16x16x32_bf16 v[58:61], v[74:77], v[86:89], v[116:119]
	v_cndmask_b32_e64 v90, 0, v169, s[6:7]
	s_mov_b32 s78, m0
	s_mov_b32 m0, s67
	s_nop 0
	global_load_lds_dwordx4 v90, s[52:53]
	s_mov_b32 m0, s78
	v_mfma_f32_16x16x32_bf16 v[112:115], v[74:77], v[120:123], v[112:115]
	s_waitcnt lgkmcnt(0)
	v_mfma_f32_16x16x32_bf16 v[116:119], v[82:85], v[86:89], v[54:57]
	s_nop 2
	ds_read_b64_tr_b16 v[54:55], v109 offset:16384
	ds_read_b64_tr_b16 v[56:57], v109 offset:17408
	v_cndmask_b32_e64 v74, 0, v170, s[6:7]
	s_mov_b32 s78, m0
	s_mov_b32 m0, s68
	s_nop 0
	global_load_lds_dwordx4 v74, s[52:53]
	s_mov_b32 m0, s78
	v_mfma_f32_16x16x32_bf16 v[34:37], v[82:85], v[120:123], v[34:37]
	ds_read_b64_tr_b16 v[74:75], v110 offset:16384
	ds_read_b64_tr_b16 v[76:77], v110 offset:17408
	s_waitcnt lgkmcnt(2)
	v_mfma_f32_16x16x32_bf16 v[30:33], v[54:57], v[86:89], v[30:33]
	v_cndmask_b32_e64 v82, 0, v174, s[6:7]
	s_mov_b32 s78, m0
	s_mov_b32 m0, s69
	s_nop 0
	global_load_lds_dwordx4 v82, s[52:53]
	s_mov_b32 m0, s78
	v_mfma_f32_16x16x32_bf16 v[14:17], v[54:57], v[120:123], v[14:17]
	ds_read_b64_tr_b16 v[54:55], v171 offset:24576
	ds_read_b64_tr_b16 v[56:57], v171 offset:25600
	ds_read_b128 v[124:127], v103
	ds_read_b128 v[136:139], v103 offset:2048
	s_waitcnt lgkmcnt(4)
	v_mfma_f32_16x16x32_bf16 v[10:13], v[74:77], v[86:89], v[10:13]
	v_cndmask_b32_e64 v82, 0, v175, s[6:7]
	s_mov_b32 s6, m0
	s_mov_b32 m0, s70
	s_nop 0
	global_load_lds_dwordx4 v82, s[52:53]
	s_mov_b32 m0, s6
	v_mfma_f32_16x16x32_bf16 v[2:5], v[74:77], v[120:123], v[2:5]
	s_waitcnt lgkmcnt(1)
	v_mfma_f32_16x16x32_bf16 v[94:97], v[54:57], v[124:127], v[46:49]
	s_nop 2
	ds_read_b64_tr_b16 v[46:47], v104 offset:24576
	ds_read_b64_tr_b16 v[48:49], v104 offset:25600
	s_waitcnt lgkmcnt(2)
	v_mfma_f32_16x16x32_bf16 v[74:77], v[54:57], v[136:139], v[62:65]
	ds_read_b64_tr_b16 v[54:55], v105 offset:24576
	ds_read_b64_tr_b16 v[56:57], v105 offset:25600
	s_waitcnt lgkmcnt(2)
	v_mfma_f32_16x16x32_bf16 v[90:93], v[46:49], v[124:127], v[78:81]
	v_mfma_f32_16x16x32_bf16 v[46:49], v[46:49], v[136:139], v[66:69]
	ds_read_b64_tr_b16 v[62:63], v106 offset:24576
	ds_read_b64_tr_b16 v[64:65], v106 offset:25600
	s_waitcnt lgkmcnt(2)
	v_mfma_f32_16x16x32_bf16 v[70:73], v[54:57], v[124:127], v[70:73]
	v_mfma_f32_16x16x32_bf16 v[18:21], v[54:57], v[136:139], v[18:21]
	ds_read_b64_tr_b16 v[54:55], v107 offset:24576
	ds_read_b64_tr_b16 v[56:57], v107 offset:25600
	s_waitcnt lgkmcnt(2)
	v_mfma_f32_16x16x32_bf16 v[42:45], v[62:65], v[124:127], v[42:45]
	v_mfma_f32_16x16x32_bf16 v[6:9], v[62:65], v[136:139], v[6:9]
	s_waitcnt lgkmcnt(0)
	v_mfma_f32_16x16x32_bf16 v[86:89], v[54:57], v[124:127], v[58:61]
	s_nop 2
	ds_read_b64_tr_b16 v[58:59], v108 offset:24576
	ds_read_b64_tr_b16 v[60:61], v108 offset:25600
	s_cbranch_vccz .Lmy_tl_272_0
	global_load_dwordx4 v[78:81], v111, s[50:51]
.Lmy_tl_272_0:
	v_mfma_f32_16x16x32_bf16 v[54:57], v[54:57], v[136:139], v[112:115]
	s_nop 2
	ds_read_b64_tr_b16 v[112:113], v109 offset:24576
	ds_read_b64_tr_b16 v[114:115], v109 offset:25600
	s_waitcnt lgkmcnt(2)
	v_mfma_f32_16x16x32_bf16 v[62:65], v[58:61], v[124:127], v[116:119]
	s_cbranch_vccz .Lmy_tl_272_1
	global_load_dwordx4 v[66:69], v111, s[50:51] offset:2048
.Lmy_tl_272_1:
	v_mfma_f32_16x16x32_bf16 v[34:37], v[58:61], v[136:139], v[34:37]
	s_nop 1
	ds_read_b64_tr_b16 v[116:117], v110 offset:24576
	ds_read_b64_tr_b16 v[118:119], v110 offset:25600
	s_waitcnt lgkmcnt(2)
	v_mfma_f32_16x16x32_bf16 v[30:33], v[112:115], v[124:127], v[30:33]
	s_add_u32 s6, s76, 0x81000
	s_addc_u32 s7, s77, 0
	s_cbranch_vccz .Lmy_tl_272_2
	global_load_dwordx4 v[82:85], v111, s[6:7]
.Lmy_tl_272_2:
	v_mfma_f32_16x16x32_bf16 v[14:17], v[112:115], v[136:139], v[14:17]
	s_waitcnt lgkmcnt(0)
	v_mfma_f32_16x16x32_bf16 v[10:13], v[116:119], v[124:127], v[10:13]
	s_cbranch_vccz .Lmy_tl_272_3
	global_load_dwordx4 v[58:61], v111, s[6:7] offset:2048
.Lmy_tl_272_3:
	v_mfma_f32_16x16x32_bf16 v[2:5], v[116:119], v[136:139], v[2:5]
	s_waitcnt lgkmcnt(0)
	s_barrier
	s_mov_b32 s52, s75
	s_cbranch_vccnz .LBB0_272
	s_waitcnt vmcnt(0)
	s_waitcnt lgkmcnt(0)
	s_barrier
	v_mov_b32_e32 v81, 0
	v_mov_b32_e32 v80, v81
	v_mov_b32_e32 v79, v81
	v_mov_b32_e32 v78, v81
	v_mov_b32_e32 v61, v81
	v_mov_b32_e32 v60, v81
	v_mov_b32_e32 v59, v81
	v_mov_b32_e32 v58, v81
	v_mov_b32_e32 v41, v81
	v_mov_b32_e32 v40, v81
	v_mov_b32_e32 v39, v81
	v_mov_b32_e32 v38, v81
	v_mov_b32_e32 v25, v81
	v_mov_b32_e32 v24, v81
	v_mov_b32_e32 v23, v81
	v_mov_b32_e32 v22, v81
	v_mov_b32_e32 v85, v81
	v_mov_b32_e32 v84, v81
	v_mov_b32_e32 v83, v81
	v_mov_b32_e32 v82, v81
	v_mov_b32_e32 v69, v81
	v_mov_b32_e32 v68, v81
	v_mov_b32_e32 v67, v81
	v_mov_b32_e32 v66, v81
	v_mov_b32_e32 v53, v81
	v_mov_b32_e32 v52, v81
	v_mov_b32_e32 v51, v81
	v_mov_b32_e32 v50, v81
	v_mov_b32_e32 v29, v81
	v_mov_b32_e32 v28, v81
	v_mov_b32_e32 v27, v81
	v_mov_b32_e32 v26, v81

.LBB0_279:
	s_waitcnt vmcnt(4)
	s_min_u32 s6, s48, 12
	ds_read_b64_tr_b16 v[196:197], v171
	ds_read_b64_tr_b16 v[198:199], v171 offset:1024
	ds_read_b128 v[200:203], v172
	ds_read_b128 v[204:207], v172 offset:2048
	ds_read_b128 v[208:211], v172 offset:4096
	ds_read_b128 v[214:217], v172 offset:6144
	s_cmp_lt_u32 s48, 13
	s_cselect_b64 vcc, -1, 0
	s_lshl_b32 s6, s6, 17
	s_add_u32 s49, s22, s6
	s_addc_u32 s79, s23, 0
	s_add_u32 s6, s49, 0x60000
	ds_read_b64_tr_b16 v[224:225], v179
	ds_read_b64_tr_b16 v[226:227], v179 offset:1024
	s_waitcnt lgkmcnt(5)
	v_mfma_f32_16x16x32_bf16 v[94:97], v[196:199], v[200:203], v[94:97]
	s_addc_u32 s7, s79, 0
	s_add_u32 s10, s18, s8
	s_addc_u32 s11, s19, s9
	s_waitcnt lgkmcnt(4)
	v_mfma_f32_16x16x32_bf16 v[74:77], v[196:199], v[204:207], v[74:77]
	s_add_u32 s10, s10, 0x80
	v_cvt_pk_bf16_f32 v138, v138, v139
	v_cvt_pk_bf16_f32 v139, v140, v141
	s_waitcnt lgkmcnt(3)
	v_mfma_f32_16x16x32_bf16 v[78:81], v[196:199], v[208:211], v[78:81]
	v_cndmask_b32_e32 v212, 0, v168, vcc
	s_addc_u32 s11, s11, 0
	ds_write_b64 v186, v[138:139] offset:16384
	s_waitcnt lgkmcnt(3)
	v_mfma_f32_16x16x32_bf16 v[122:125], v[196:199], v[214:217], v[122:125]
	ds_read_b64_tr_b16 v[138:139], v180
	ds_read_b64_tr_b16 v[140:141], v180 offset:1024
	s_waitcnt lgkmcnt(3)
	v_mfma_f32_16x16x32_bf16 v[90:93], v[224:227], v[200:203], v[90:93]
	v_cvt_pk_bf16_f32 v134, v134, v135
	v_cvt_pk_bf16_f32 v135, v136, v137
	ds_write_b64 v193, v[134:135] offset:16640
	v_mfma_f32_16x16x32_bf16 v[46:49], v[224:227], v[204:207], v[46:49]
	v_mfma_f32_16x16x32_bf16 v[58:61], v[224:227], v[208:211], v[58:61]
	v_mfma_f32_16x16x32_bf16 v[114:117], v[224:227], v[214:217], v[114:117]
	ds_read_b64_tr_b16 v[134:135], v181
	ds_read_b64_tr_b16 v[136:137], v181 offset:1024
	s_waitcnt lgkmcnt(3)
	v_mfma_f32_16x16x32_bf16 v[70:73], v[138:141], v[200:203], v[70:73]
	v_cvt_pk_bf16_f32 v142, v142, v143
	v_cvt_pk_bf16_f32 v143, v144, v145
	ds_write_b64 v194, v[142:143] offset:16896
	v_mfma_f32_16x16x32_bf16 v[18:21], v[138:141], v[204:207], v[18:21]
	v_mfma_f32_16x16x32_bf16 v[38:41], v[138:141], v[208:211], v[38:41]
	v_mfma_f32_16x16x32_bf16 v[106:109], v[138:141], v[214:217], v[106:109]
	ds_read_b64_tr_b16 v[138:139], v182
	ds_read_b64_tr_b16 v[140:141], v182 offset:1024
	s_waitcnt lgkmcnt(3)
	v_mfma_f32_16x16x32_bf16 v[42:45], v[134:137], v[200:203], v[42:45]
	v_cvt_pk_bf16_f32 v130, v130, v131
	v_cvt_pk_bf16_f32 v131, v132, v133
	ds_write_b64 v195, v[130:131] offset:17152
	v_mfma_f32_16x16x32_bf16 v[6:9], v[134:137], v[204:207], v[6:9]
	v_mfma_f32_16x16x32_bf16 v[22:25], v[134:137], v[208:211], v[22:25]
	v_mfma_f32_16x16x32_bf16 v[102:105], v[134:137], v[214:217], v[102:105]
	ds_read_b64_tr_b16 v[130:131], v183
	ds_read_b64_tr_b16 v[132:133], v183 offset:1024
	s_waitcnt lgkmcnt(3)
	v_mfma_f32_16x16x32_bf16 v[86:89], v[138:141], v[200:203], v[86:89]
	s_mov_b32 s80, m0
	s_mov_b32 m0, s71
	s_nop 0
	global_load_lds_dwordx4 v169, s[10:11]
	s_mov_b32 m0, s80
	v_mfma_f32_16x16x32_bf16 v[54:57], v[138:141], v[204:207], v[54:57]
	v_mfma_f32_16x16x32_bf16 v[82:85], v[138:141], v[208:211], v[82:85]
	v_mfma_f32_16x16x32_bf16 v[126:129], v[138:141], v[214:217], v[126:129]
	ds_read_b64_tr_b16 v[134:135], v184
	ds_read_b64_tr_b16 v[136:137], v184 offset:1024
	s_waitcnt lgkmcnt(2)
	v_mfma_f32_16x16x32_bf16 v[62:65], v[130:133], v[200:203], v[62:65]
	s_mov_b32 s80, m0
	s_mov_b32 m0, s72
	s_nop 0
	global_load_lds_dwordx4 v170, s[10:11]
	s_mov_b32 m0, s80
	v_mfma_f32_16x16x32_bf16 v[34:37], v[130:133], v[204:207], v[34:37]
	v_mfma_f32_16x16x32_bf16 v[66:69], v[130:133], v[208:211], v[66:69]
	v_mfma_f32_16x16x32_bf16 v[118:121], v[130:133], v[214:217], v[118:121]
	ds_read_b64_tr_b16 v[130:131], v185
	ds_read_b64_tr_b16 v[132:133], v185 offset:1024
	s_waitcnt lgkmcnt(2)
	v_mfma_f32_16x16x32_bf16 v[30:33], v[134:137], v[200:203], v[30:33]
	s_mov_b32 s80, m0
	s_mov_b32 m0, s73
	s_nop 0
	global_load_lds_dwordx4 v174, s[10:11]
	s_mov_b32 m0, s80
	v_mfma_f32_16x16x32_bf16 v[14:17], v[134:137], v[204:207], v[14:17]
	v_mfma_f32_16x16x32_bf16 v[50:53], v[134:137], v[208:211], v[50:53]
	v_mfma_f32_16x16x32_bf16 v[110:113], v[134:137], v[214:217], v[110:113]
	s_waitcnt lgkmcnt(0)
	v_mfma_f32_16x16x32_bf16 v[10:13], v[130:133], v[200:203], v[10:13]
	ds_read_b64_tr_b16 v[134:135], v171 offset:8192
	ds_read_b64_tr_b16 v[136:137], v171 offset:9216
	v_mfma_f32_16x16x32_bf16 v[2:5], v[130:133], v[204:207], v[2:5]
	v_mfma_f32_16x16x32_bf16 v[26:29], v[130:133], v[208:211], v[26:29]
	ds_read_b128 v[196:199], v178
	ds_read_b128 v[200:203], v178 offset:2048
	ds_read_b128 v[204:207], v178 offset:4096
	ds_read_b128 v[208:211], v178 offset:6144
	s_mov_b32 s80, m0
	s_mov_b32 m0, s74
	s_nop 0
	global_load_lds_dwordx4 v175, s[10:11]
	s_mov_b32 m0, s80
	v_mfma_f32_16x16x32_bf16 v[98:101], v[130:133], v[214:217], v[98:101]
	ds_read_b64_tr_b16 v[130:131], v179 offset:8192
	ds_read_b64_tr_b16 v[132:133], v179 offset:9216
	s_waitcnt lgkmcnt(5)
	v_mfma_f32_16x16x32_bf16 v[94:97], v[134:137], v[196:199], v[94:97]
	s_mov_b32 s80, m0
	s_mov_b32 m0, s75
	s_nop 0
	global_load_lds_dwordx4 v176, s[10:11]
	s_mov_b32 m0, s80
	s_waitcnt lgkmcnt(4)
	v_mfma_f32_16x16x32_bf16 v[74:77], v[134:137], v[200:203], v[74:77]
	s_waitcnt lgkmcnt(3)
	v_mfma_f32_16x16x32_bf16 v[78:81], v[134:137], v[204:207], v[78:81]
	s_waitcnt lgkmcnt(2)
	v_mfma_f32_16x16x32_bf16 v[122:125], v[134:137], v[208:211], v[122:125]
	ds_read_b64_tr_b16 v[134:135], v180 offset:8192
	ds_read_b64_tr_b16 v[136:137], v180 offset:9216
	s_waitcnt lgkmcnt(2)
	v_mfma_f32_16x16x32_bf16 v[90:93], v[130:133], v[196:199], v[90:93]
	s_mov_b32 s80, m0
	s_mov_b32 m0, s76
	s_nop 0
	global_load_lds_dwordx4 v177, s[10:11]
	s_mov_b32 m0, s80
	v_mfma_f32_16x16x32_bf16 v[46:49], v[130:133], v[200:203], v[46:49]
	v_mfma_f32_16x16x32_bf16 v[58:61], v[130:133], v[204:207], v[58:61]
	v_mfma_f32_16x16x32_bf16 v[114:117], v[130:133], v[208:211], v[114:117]
	ds_read_b64_tr_b16 v[130:131], v181 offset:8192
	ds_read_b64_tr_b16 v[132:133], v181 offset:9216
	s_waitcnt lgkmcnt(2)
	v_mfma_f32_16x16x32_bf16 v[70:73], v[134:137], v[196:199], v[70:73]
	s_mov_b32 s80, m0
	s_mov_b32 m0, s77
	s_nop 0
	global_load_lds_dwordx4 v191, s[10:11]
	s_mov_b32 m0, s80
	v_mfma_f32_16x16x32_bf16 v[18:21], v[134:137], v[200:203], v[18:21]
	v_mfma_f32_16x16x32_bf16 v[38:41], v[134:137], v[204:207], v[38:41]
	v_mfma_f32_16x16x32_bf16 v[106:109], v[134:137], v[208:211], v[106:109]
	ds_read_b64_tr_b16 v[134:135], v182 offset:8192
	ds_read_b64_tr_b16 v[136:137], v182 offset:9216
	s_waitcnt lgkmcnt(2)
	v_mfma_f32_16x16x32_bf16 v[42:45], v[130:133], v[196:199], v[42:45]
	s_mov_b32 s80, m0
	s_mov_b32 m0, s78
	s_nop 0
	global_load_lds_dwordx4 v192, s[10:11]
	s_mov_b32 m0, s80
	v_mfma_f32_16x16x32_bf16 v[6:9], v[130:133], v[200:203], v[6:9]
	v_mfma_f32_16x16x32_bf16 v[22:25], v[130:133], v[204:207], v[22:25]
	v_mfma_f32_16x16x32_bf16 v[102:105], v[130:133], v[208:211], v[102:105]
	ds_read_b64_tr_b16 v[130:131], v183 offset:8192
	ds_read_b64_tr_b16 v[132:133], v183 offset:9216
	s_waitcnt lgkmcnt(2)
	v_mfma_f32_16x16x32_bf16 v[86:89], v[134:137], v[196:199], v[86:89]
	global_load_dwordx4 v[138:141], v212, s[6:7]
	v_mfma_f32_16x16x32_bf16 v[54:57], v[134:137], v[200:203], v[54:57]
	v_mfma_f32_16x16x32_bf16 v[82:85], v[134:137], v[204:207], v[82:85]
	v_mfma_f32_16x16x32_bf16 v[126:129], v[134:137], v[208:211], v[126:129]
	ds_read_b64_tr_b16 v[214:215], v184 offset:8192
	ds_read_b64_tr_b16 v[216:217], v184 offset:9216
	s_waitcnt lgkmcnt(2)
	v_mfma_f32_16x16x32_bf16 v[62:65], v[130:133], v[196:199], v[62:65]
	global_load_dwordx4 v[134:137], v212, s[6:7] offset:2048
	v_mfma_f32_16x16x32_bf16 v[34:37], v[130:133], v[200:203], v[34:37]
	v_mfma_f32_16x16x32_bf16 v[66:69], v[130:133], v[204:207], v[66:69]
	v_mfma_f32_16x16x32_bf16 v[118:121], v[130:133], v[208:211], v[118:121]
	ds_read_b64_tr_b16 v[224:225], v185 offset:8192
	ds_read_b64_tr_b16 v[226:227], v185 offset:9216
	s_waitcnt lgkmcnt(2)
	v_mfma_f32_16x16x32_bf16 v[30:33], v[214:217], v[196:199], v[30:33]
	s_add_u32 s6, s49, 0x61000
	s_addc_u32 s7, s79, 0
	global_load_dwordx4 v[142:145], v212, s[6:7]
	v_mfma_f32_16x16x32_bf16 v[14:17], v[214:217], v[200:203], v[14:17]
	v_mfma_f32_16x16x32_bf16 v[50:53], v[214:217], v[204:207], v[50:53]
	v_mfma_f32_16x16x32_bf16 v[110:113], v[214:217], v[208:211], v[110:113]
	s_waitcnt lgkmcnt(0)
	v_mfma_f32_16x16x32_bf16 v[10:13], v[224:227], v[196:199], v[10:13]
	global_load_dwordx4 v[130:133], v212, s[6:7] offset:2048
	v_mfma_f32_16x16x32_bf16 v[2:5], v[224:227], v[200:203], v[2:5]
	v_mfma_f32_16x16x32_bf16 v[26:29], v[224:227], v[204:207], v[26:29]
	v_mfma_f32_16x16x32_bf16 v[98:101], v[224:227], v[208:211], v[98:101]
	s_min_u32 s6, s48, 11
	s_add_i32 s79, s48, 2
	s_cmp_lt_u32 s48, 12
	s_cselect_b64 vcc, -1, 0
	s_lshl_b32 s6, s6, 17
	s_waitcnt lgkmcnt(0)
	s_barrier
	s_add_u32 s80, s22, s6
	s_waitcnt vmcnt(4)
	s_addc_u32 s81, s23, 0
	ds_read_b64_tr_b16 v[196:197], v171 offset:16384
	ds_read_b64_tr_b16 v[198:199], v171 offset:17408
	s_add_u32 s10, s80, 0x80000
	ds_read_b128 v[200:203], v172 offset:8192
	ds_read_b128 v[204:207], v172 offset:10240
	ds_read_b128 v[208:211], v172 offset:12288
	ds_read_b128 v[214:217], v172 offset:14336
	s_addc_u32 s11, s81, 0
	s_add_u32 s8, s8, 0x100
	s_addc_u32 s9, s9, 0
	s_cmp_lt_u32 s48, 14
	ds_read_b64_tr_b16 v[224:225], v179 offset:16384
	ds_read_b64_tr_b16 v[226:227], v179 offset:17408
	s_cselect_b64 s[6:7], -1, 0
	s_waitcnt lgkmcnt(5)
	v_mfma_f32_16x16x32_bf16 v[94:97], v[196:199], v[200:203], v[94:97]
	v_cndmask_b32_e32 v212, 0, v168, vcc
	s_and_b64 vcc, s[6:7], exec
	s_cselect_b32 s48, s8, 0x780
	s_waitcnt lgkmcnt(4)
	v_mfma_f32_16x16x32_bf16 v[74:77], v[196:199], v[204:207], v[74:77]
	s_add_u32 s48, s18, s48
	v_cvt_pk_bf16_f32 v154, v154, v155
	v_cvt_pk_bf16_f32 v155, v156, v157
	s_waitcnt lgkmcnt(3)
	v_mfma_f32_16x16x32_bf16 v[78:81], v[196:199], v[208:211], v[78:81]
	s_addc_u32 s49, s19, 0
	ds_write_b64 v186, v[154:155]
	s_waitcnt lgkmcnt(3)
	v_mfma_f32_16x16x32_bf16 v[122:125], v[196:199], v[214:217], v[122:125]
	ds_read_b64_tr_b16 v[154:155], v180 offset:16384
	ds_read_b64_tr_b16 v[156:157], v180 offset:17408
	s_waitcnt lgkmcnt(3)
	v_mfma_f32_16x16x32_bf16 v[90:93], v[224:227], v[200:203], v[90:93]
	v_cvt_pk_bf16_f32 v150, v150, v151
	v_cvt_pk_bf16_f32 v151, v152, v153
	ds_write_b64 v193, v[150:151] offset:256
	v_mfma_f32_16x16x32_bf16 v[46:49], v[224:227], v[204:207], v[46:49]
	v_mfma_f32_16x16x32_bf16 v[58:61], v[224:227], v[208:211], v[58:61]
	v_mfma_f32_16x16x32_bf16 v[114:117], v[224:227], v[214:217], v[114:117]
	ds_read_b64_tr_b16 v[150:151], v181 offset:16384
	ds_read_b64_tr_b16 v[152:153], v181 offset:17408
	s_waitcnt lgkmcnt(3)
	v_mfma_f32_16x16x32_bf16 v[70:73], v[154:157], v[200:203], v[70:73]
	v_cvt_pk_bf16_f32 v158, v158, v159
	v_cvt_pk_bf16_f32 v159, v160, v161
	ds_write_b64 v194, v[158:159] offset:512
	v_mfma_f32_16x16x32_bf16 v[18:21], v[154:157], v[204:207], v[18:21]
	v_mfma_f32_16x16x32_bf16 v[38:41], v[154:157], v[208:211], v[38:41]
	v_mfma_f32_16x16x32_bf16 v[106:109], v[154:157], v[214:217], v[106:109]
	ds_read_b64_tr_b16 v[154:155], v182 offset:16384
	ds_read_b64_tr_b16 v[156:157], v182 offset:17408
	s_waitcnt lgkmcnt(3)
	v_mfma_f32_16x16x32_bf16 v[42:45], v[150:153], v[200:203], v[42:45]
	v_cvt_pk_bf16_f32 v146, v146, v147
	v_cvt_pk_bf16_f32 v147, v148, v149
	ds_write_b64 v195, v[146:147] offset:768
	v_mfma_f32_16x16x32_bf16 v[6:9], v[150:153], v[204:207], v[6:9]
	v_mfma_f32_16x16x32_bf16 v[22:25], v[150:153], v[208:211], v[22:25]
	v_mfma_f32_16x16x32_bf16 v[102:105], v[150:153], v[214:217], v[102:105]
	ds_read_b64_tr_b16 v[146:147], v183 offset:16384
	ds_read_b64_tr_b16 v[148:149], v183 offset:17408
	s_waitcnt lgkmcnt(3)
	v_mfma_f32_16x16x32_bf16 v[86:89], v[154:157], v[200:203], v[86:89]
	v_cndmask_b32_e64 v150, 0, v169, s[6:7]
	s_mov_b32 s82, m0
	s_mov_b32 m0, s67
	s_nop 0
	global_load_lds_dwordx4 v150, s[48:49]
	s_mov_b32 m0, s82
	v_mfma_f32_16x16x32_bf16 v[54:57], v[154:157], v[204:207], v[54:57]
	v_mfma_f32_16x16x32_bf16 v[82:85], v[154:157], v[208:211], v[82:85]
	v_mfma_f32_16x16x32_bf16 v[126:129], v[154:157], v[214:217], v[126:129]
	ds_read_b64_tr_b16 v[150:151], v184 offset:16384
	ds_read_b64_tr_b16 v[152:153], v184 offset:17408
	s_waitcnt lgkmcnt(2)
	v_mfma_f32_16x16x32_bf16 v[62:65], v[146:149], v[200:203], v[62:65]
	v_cndmask_b32_e64 v154, 0, v170, s[6:7]
	s_mov_b32 s82, m0
	s_mov_b32 m0, s68
	s_nop 0
	global_load_lds_dwordx4 v154, s[48:49]
	s_mov_b32 m0, s82
	v_mfma_f32_16x16x32_bf16 v[34:37], v[146:149], v[204:207], v[34:37]
	v_mfma_f32_16x16x32_bf16 v[66:69], v[146:149], v[208:211], v[66:69]
	v_mfma_f32_16x16x32_bf16 v[118:121], v[146:149], v[214:217], v[118:121]
	ds_read_b64_tr_b16 v[146:147], v185 offset:16384
	ds_read_b64_tr_b16 v[148:149], v185 offset:17408
	s_waitcnt lgkmcnt(2)
	v_mfma_f32_16x16x32_bf16 v[30:33], v[150:153], v[200:203], v[30:33]
	v_cndmask_b32_e64 v154, 0, v174, s[6:7]
	s_mov_b32 s82, m0
	s_mov_b32 m0, s50
	s_nop 0
	global_load_lds_dwordx4 v154, s[48:49]
	s_mov_b32 m0, s82
	v_mfma_f32_16x16x32_bf16 v[14:17], v[150:153], v[204:207], v[14:17]
	v_mfma_f32_16x16x32_bf16 v[50:53], v[150:153], v[208:211], v[50:53]
	v_mfma_f32_16x16x32_bf16 v[110:113], v[150:153], v[214:217], v[110:113]
	s_waitcnt lgkmcnt(0)
	v_mfma_f32_16x16x32_bf16 v[10:13], v[146:149], v[200:203], v[10:13]
	ds_read_b64_tr_b16 v[150:151], v171 offset:24576
	ds_read_b64_tr_b16 v[152:153], v171 offset:25600
	ds_read_b128 v[196:199], v187
	ds_read_b128 v[200:203], v187 offset:2048
	v_cndmask_b32_e64 v154, 0, v175, s[6:7]
	v_mfma_f32_16x16x32_bf16 v[2:5], v[146:149], v[204:207], v[2:5]
	v_mfma_f32_16x16x32_bf16 v[26:29], v[146:149], v[208:211], v[26:29]
	ds_read_b128 v[204:207], v187 offset:4096
	ds_read_b128 v[208:211], v187 offset:6144
	s_mov_b32 s82, m0
	s_mov_b32 m0, s51
	s_nop 0
	global_load_lds_dwordx4 v154, s[48:49]
	s_mov_b32 m0, s82
	v_mfma_f32_16x16x32_bf16 v[98:101], v[146:149], v[214:217], v[98:101]
	ds_read_b64_tr_b16 v[146:147], v179 offset:24576
	ds_read_b64_tr_b16 v[148:149], v179 offset:25600
	s_waitcnt lgkmcnt(5)
	v_mfma_f32_16x16x32_bf16 v[94:97], v[150:153], v[196:199], v[94:97]
	v_cndmask_b32_e64 v154, 0, v176, s[6:7]
	s_mov_b32 s82, m0
	s_mov_b32 m0, s52
	s_nop 0
	global_load_lds_dwordx4 v154, s[48:49]
	s_mov_b32 m0, s82
	s_waitcnt lgkmcnt(4)
	v_mfma_f32_16x16x32_bf16 v[74:77], v[150:153], v[200:203], v[74:77]
	s_waitcnt lgkmcnt(3)
	v_mfma_f32_16x16x32_bf16 v[78:81], v[150:153], v[204:207], v[78:81]
	s_waitcnt lgkmcnt(2)
	v_mfma_f32_16x16x32_bf16 v[122:125], v[150:153], v[208:211], v[122:125]
	ds_read_b64_tr_b16 v[150:151], v180 offset:24576
	ds_read_b64_tr_b16 v[152:153], v180 offset:25600
	s_waitcnt lgkmcnt(2)
	v_mfma_f32_16x16x32_bf16 v[90:93], v[146:149], v[196:199], v[90:93]
	v_cndmask_b32_e64 v154, 0, v177, s[6:7]
	s_mov_b32 s82, m0
	s_mov_b32 m0, s53
	s_nop 0
	global_load_lds_dwordx4 v154, s[48:49]
	s_mov_b32 m0, s82
	v_mfma_f32_16x16x32_bf16 v[46:49], v[146:149], v[200:203], v[46:49]
	v_mfma_f32_16x16x32_bf16 v[58:61], v[146:149], v[204:207], v[58:61]
	v_mfma_f32_16x16x32_bf16 v[114:117], v[146:149], v[208:211], v[114:117]
	ds_read_b64_tr_b16 v[146:147], v181 offset:24576
	ds_read_b64_tr_b16 v[148:149], v181 offset:25600
	s_waitcnt lgkmcnt(2)
	v_mfma_f32_16x16x32_bf16 v[70:73], v[150:153], v[196:199], v[70:73]
	v_cndmask_b32_e64 v154, 0, v191, s[6:7]
	s_mov_b32 s82, m0
	s_mov_b32 m0, s69
	s_nop 0
	global_load_lds_dwordx4 v154, s[48:49]
	s_mov_b32 m0, s82
	v_mfma_f32_16x16x32_bf16 v[18:21], v[150:153], v[200:203], v[18:21]
	v_mfma_f32_16x16x32_bf16 v[38:41], v[150:153], v[204:207], v[38:41]
	v_mfma_f32_16x16x32_bf16 v[106:109], v[150:153], v[208:211], v[106:109]
	ds_read_b64_tr_b16 v[150:151], v182 offset:24576
	ds_read_b64_tr_b16 v[152:153], v182 offset:25600
	s_waitcnt lgkmcnt(2)
	v_mfma_f32_16x16x32_bf16 v[42:45], v[146:149], v[196:199], v[42:45]
	v_cndmask_b32_e64 v154, 0, v192, s[6:7]
	s_mov_b32 s6, m0
	s_mov_b32 m0, s70
	s_nop 0
	global_load_lds_dwordx4 v154, s[48:49]
	s_mov_b32 m0, s6
	v_mfma_f32_16x16x32_bf16 v[6:9], v[146:149], v[200:203], v[6:9]
	v_mfma_f32_16x16x32_bf16 v[22:25], v[146:149], v[204:207], v[22:25]
	v_mfma_f32_16x16x32_bf16 v[102:105], v[146:149], v[208:211], v[102:105]
	ds_read_b64_tr_b16 v[146:147], v183 offset:24576
	ds_read_b64_tr_b16 v[148:149], v183 offset:25600
	s_waitcnt lgkmcnt(2)
	v_mfma_f32_16x16x32_bf16 v[86:89], v[150:153], v[196:199], v[86:89]
	s_cbranch_vccz .Lmy_tl_279_0
	global_load_dwordx4 v[154:157], v212, s[10:11]
.Lmy_tl_279_0:
	v_mfma_f32_16x16x32_bf16 v[54:57], v[150:153], v[200:203], v[54:57]
	v_mfma_f32_16x16x32_bf16 v[82:85], v[150:153], v[204:207], v[82:85]
	v_mfma_f32_16x16x32_bf16 v[126:129], v[150:153], v[208:211], v[126:129]
	ds_read_b64_tr_b16 v[214:215], v184 offset:24576
	ds_read_b64_tr_b16 v[216:217], v184 offset:25600
	s_waitcnt lgkmcnt(2)
	v_mfma_f32_16x16x32_bf16 v[62:65], v[146:149], v[196:199], v[62:65]
	s_cbranch_vccz .Lmy_tl_279_1
	global_load_dwordx4 v[150:153], v212, s[10:11] offset:2048
.Lmy_tl_279_1:
	v_mfma_f32_16x16x32_bf16 v[34:37], v[146:149], v[200:203], v[34:37]
	v_mfma_f32_16x16x32_bf16 v[66:69], v[146:149], v[204:207], v[66:69]
	v_mfma_f32_16x16x32_bf16 v[118:121], v[146:149], v[208:211], v[118:121]
	ds_read_b64_tr_b16 v[224:225], v185 offset:24576
	ds_read_b64_tr_b16 v[226:227], v185 offset:25600
	s_waitcnt lgkmcnt(2)
	v_mfma_f32_16x16x32_bf16 v[30:33], v[214:217], v[196:199], v[30:33]
	s_add_u32 s6, s80, 0x81000
	s_addc_u32 s7, s81, 0
	s_cbranch_vccz .Lmy_tl_279_2
	global_load_dwordx4 v[158:161], v212, s[6:7]
.Lmy_tl_279_2:
	v_mfma_f32_16x16x32_bf16 v[14:17], v[214:217], v[200:203], v[14:17]
	v_mfma_f32_16x16x32_bf16 v[50:53], v[214:217], v[204:207], v[50:53]
	v_mfma_f32_16x16x32_bf16 v[110:113], v[214:217], v[208:211], v[110:113]
	s_waitcnt lgkmcnt(0)
	v_mfma_f32_16x16x32_bf16 v[10:13], v[224:227], v[196:199], v[10:13]
	s_cbranch_vccz .Lmy_tl_279_3
	global_load_dwordx4 v[146:149], v212, s[6:7] offset:2048
.Lmy_tl_279_3:
	v_mfma_f32_16x16x32_bf16 v[2:5], v[224:227], v[200:203], v[2:5]
	v_mfma_f32_16x16x32_bf16 v[26:29], v[224:227], v[204:207], v[26:29]
	v_mfma_f32_16x16x32_bf16 v[98:101], v[224:227], v[208:211], v[98:101]
	s_waitcnt lgkmcnt(0)
	s_barrier
	s_mov_b32 s48, s79
	s_cbranch_vccnz .LBB0_279
	s_waitcnt vmcnt(0)
	s_waitcnt lgkmcnt(0)
	s_barrier
	s_mov_b64 s[8:9], 0

.LBB0_283:
	s_cmp_lt_u32 s50, 13
	s_cselect_b64 vcc, -1, 0
	s_min_u32 s6, s50, 12
	s_lshl_b32 s6, s6, 17
	s_add_u32 s51, s22, s6
	s_waitcnt vmcnt(4)
	s_addc_u32 s52, s23, 0
	ds_read_b128 v[50:53], v172
	ds_read_b64_tr_b16 v[54:55], v171
	ds_read_b64_tr_b16 v[56:57], v171 offset:1024
	s_add_u32 s6, s51, 0x60000
	ds_read_b64_tr_b16 v[58:59], v179
	ds_read_b64_tr_b16 v[60:61], v179 offset:1024
	s_addc_u32 s7, s52, 0
	s_add_u32 s10, s18, s8
	s_addc_u32 s11, s19, s9
	s_add_u32 s10, s10, 0x80
	v_cvt_pk_bf16_f32 v18, v18, v19
	v_cvt_pk_bf16_f32 v19, v20, v21
	v_cndmask_b32_e32 v49, 0, v168, vcc
	s_addc_u32 s11, s11, 0
	s_waitcnt lgkmcnt(2)
	v_mfma_f32_16x16x32_bf16 v[54:57], v[54:57], v[50:53], v[94:97]
	ds_write_b64 v186, v[18:19] offset:16384
	ds_read_b64_tr_b16 v[18:19], v180
	ds_read_b64_tr_b16 v[20:21], v180 offset:1024
	v_cvt_pk_bf16_f32 v6, v6, v7
	v_cvt_pk_bf16_f32 v7, v8, v9
	s_waitcnt lgkmcnt(3)
	v_mfma_f32_16x16x32_bf16 v[58:61], v[58:61], v[50:53], v[90:93]
	ds_write_b64 v46, v[6:7] offset:16640
	ds_read_b64_tr_b16 v[6:7], v181
	ds_read_b64_tr_b16 v[8:9], v181 offset:1024
	s_waitcnt lgkmcnt(3)
	v_mfma_f32_16x16x32_bf16 v[18:21], v[18:21], v[50:53], v[70:73]
	v_cvt_pk_bf16_f32 v14, v14, v15
	v_cvt_pk_bf16_f32 v15, v16, v17
	ds_write_b64 v47, v[14:15] offset:16896
	ds_read_b64_tr_b16 v[14:15], v182
	ds_read_b64_tr_b16 v[16:17], v182 offset:1024
	s_waitcnt lgkmcnt(3)
	v_mfma_f32_16x16x32_bf16 v[6:9], v[6:9], v[50:53], v[42:45]
	v_cvt_pk_bf16_f32 v2, v2, v3
	v_cvt_pk_bf16_f32 v3, v4, v5
	ds_write_b64 v48, v[2:3] offset:17152
	ds_read_b64_tr_b16 v[2:3], v183
	ds_read_b64_tr_b16 v[4:5], v183 offset:1024
	s_waitcnt lgkmcnt(3)
	v_mfma_f32_16x16x32_bf16 v[14:17], v[14:17], v[50:53], v[86:89]
	s_mov_b32 s53, m0
	s_mov_b32 m0, s48
	s_nop 0
	global_load_lds_dwordx4 v169, s[10:11]
	s_mov_b32 m0, s53
	ds_read_b64_tr_b16 v[42:43], v184
	ds_read_b64_tr_b16 v[44:45], v184 offset:1024
	s_waitcnt lgkmcnt(2)
	v_mfma_f32_16x16x32_bf16 v[2:5], v[2:5], v[50:53], v[62:65]
	s_mov_b32 s53, m0
	s_mov_b32 m0, s49
	s_nop 0
	global_load_lds_dwordx4 v170, s[10:11]
	s_mov_b32 m0, s53
	s_nop 2
	ds_read_b64_tr_b16 v[62:63], v185
	ds_read_b64_tr_b16 v[64:65], v185 offset:1024
	s_waitcnt lgkmcnt(2)
	v_mfma_f32_16x16x32_bf16 v[30:33], v[42:45], v[50:53], v[30:33]
	ds_read_b64_tr_b16 v[42:43], v171 offset:8192
	ds_read_b64_tr_b16 v[44:45], v171 offset:9216
	ds_read_b128 v[66:69], v178
	s_waitcnt lgkmcnt(3)
	v_mfma_f32_16x16x32_bf16 v[10:13], v[62:65], v[50:53], v[10:13]
	ds_read_b64_tr_b16 v[50:51], v179 offset:8192
	ds_read_b64_tr_b16 v[52:53], v179 offset:9216
	s_waitcnt lgkmcnt(2)
	v_mfma_f32_16x16x32_bf16 v[42:45], v[42:45], v[66:69], v[54:57]
	s_nop 2
	ds_read_b64_tr_b16 v[54:55], v180 offset:8192
	ds_read_b64_tr_b16 v[56:57], v180 offset:9216
	s_waitcnt lgkmcnt(2)
	v_mfma_f32_16x16x32_bf16 v[50:53], v[50:53], v[66:69], v[58:61]
	s_nop 2
	ds_read_b64_tr_b16 v[58:59], v181 offset:8192
	ds_read_b64_tr_b16 v[60:61], v181 offset:9216
	s_waitcnt lgkmcnt(2)
	v_mfma_f32_16x16x32_bf16 v[54:57], v[54:57], v[66:69], v[18:21]
	s_nop 2
	ds_read_b64_tr_b16 v[18:19], v182 offset:8192
	ds_read_b64_tr_b16 v[20:21], v182 offset:9216
	s_waitcnt lgkmcnt(2)
	v_mfma_f32_16x16x32_bf16 v[58:61], v[58:61], v[66:69], v[6:9]
	s_nop 2
	ds_read_b64_tr_b16 v[6:7], v183 offset:8192
	ds_read_b64_tr_b16 v[8:9], v183 offset:9216
	s_waitcnt lgkmcnt(2)
	v_mfma_f32_16x16x32_bf16 v[62:65], v[18:21], v[66:69], v[14:17]
	global_load_dwordx4 v[18:21], v49, s[6:7]
	s_nop 2
	ds_read_b64_tr_b16 v[14:15], v184 offset:8192
	ds_read_b64_tr_b16 v[16:17], v184 offset:9216
	s_waitcnt lgkmcnt(2)
	v_mfma_f32_16x16x32_bf16 v[70:73], v[6:9], v[66:69], v[2:5]
	global_load_dwordx4 v[6:9], v49, s[6:7] offset:2048
	ds_read_b64_tr_b16 v[74:75], v185 offset:8192
	ds_read_b64_tr_b16 v[76:77], v185 offset:9216
	s_waitcnt lgkmcnt(2)
	v_mfma_f32_16x16x32_bf16 v[30:33], v[14:17], v[66:69], v[30:33]
	s_add_u32 s6, s51, 0x61000
	s_addc_u32 s7, s52, 0
	global_load_dwordx4 v[14:17], v49, s[6:7]
	s_waitcnt lgkmcnt(0)
	v_mfma_f32_16x16x32_bf16 v[10:13], v[74:77], v[66:69], v[10:13]
	global_load_dwordx4 v[2:5], v49, s[6:7] offset:2048
	s_add_i32 s51, s50, 2
	s_cmp_lt_u32 s50, 12
	s_cselect_b64 vcc, -1, 0
	s_min_u32 s6, s50, 11
	s_lshl_b32 s6, s6, 17
	s_waitcnt lgkmcnt(0)
	s_barrier
	s_add_u32 s69, s22, s6
	s_waitcnt vmcnt(4)
	s_addc_u32 s70, s23, 0
	s_add_u32 s10, s69, 0x80000
	ds_read_b64_tr_b16 v[66:67], v171 offset:16384
	ds_read_b64_tr_b16 v[68:69], v171 offset:17408
	ds_read_b128 v[74:77], v172 offset:8192
	s_addc_u32 s11, s70, 0
	s_add_u32 s8, s8, 0x100
	s_addc_u32 s9, s9, 0
	s_cmp_lt_u32 s50, 14
	ds_read_b64_tr_b16 v[78:79], v179 offset:16384
	ds_read_b64_tr_b16 v[80:81], v179 offset:17408
	s_cselect_b64 s[6:7], -1, 0
	s_waitcnt lgkmcnt(2)
	v_mfma_f32_16x16x32_bf16 v[42:45], v[66:69], v[74:77], v[42:45]
	v_cndmask_b32_e32 v49, 0, v168, vcc
	s_and_b64 vcc, s[6:7], exec
	s_cselect_b32 s50, s8, 0x780
	s_add_u32 s52, s18, s50
	v_cvt_pk_bf16_f32 v38, v38, v39
	v_cvt_pk_bf16_f32 v39, v40, v41
	s_addc_u32 s53, s19, 0
	ds_write_b64 v186, v[38:39]
	ds_read_b64_tr_b16 v[38:39], v180 offset:16384
	ds_read_b64_tr_b16 v[40:41], v180 offset:17408
	v_cvt_pk_bf16_f32 v26, v26, v27
	v_cvt_pk_bf16_f32 v27, v28, v29
	s_waitcnt lgkmcnt(3)
	v_mfma_f32_16x16x32_bf16 v[50:53], v[78:81], v[74:77], v[50:53]
	ds_write_b64 v46, v[26:27] offset:256
	ds_read_b64_tr_b16 v[26:27], v181 offset:16384
	ds_read_b64_tr_b16 v[28:29], v181 offset:17408
	s_waitcnt lgkmcnt(3)
	v_mfma_f32_16x16x32_bf16 v[38:41], v[38:41], v[74:77], v[54:57]
	v_cvt_pk_bf16_f32 v34, v34, v35
	v_cvt_pk_bf16_f32 v35, v36, v37
	ds_write_b64 v47, v[34:35] offset:512
	ds_read_b64_tr_b16 v[34:35], v182 offset:16384
	ds_read_b64_tr_b16 v[36:37], v182 offset:17408
	s_waitcnt lgkmcnt(3)
	v_mfma_f32_16x16x32_bf16 v[26:29], v[26:29], v[74:77], v[58:61]
	v_cvt_pk_bf16_f32 v22, v22, v23
	v_cvt_pk_bf16_f32 v23, v24, v25
	ds_write_b64 v48, v[22:23] offset:768
	ds_read_b64_tr_b16 v[22:23], v183 offset:16384
	ds_read_b64_tr_b16 v[24:25], v183 offset:17408
	s_waitcnt lgkmcnt(3)
	v_mfma_f32_16x16x32_bf16 v[34:37], v[34:37], v[74:77], v[62:65]
	v_cndmask_b32_e64 v54, 0, v169, s[6:7]
	s_mov_b32 s50, m0
	s_mov_b32 m0, s67
	s_nop 0
	global_load_lds_dwordx4 v54, s[52:53]
	s_mov_b32 m0, s50
	ds_read_b64_tr_b16 v[54:55], v184 offset:16384
	ds_read_b64_tr_b16 v[56:57], v184 offset:17408
	s_waitcnt lgkmcnt(2)
	v_mfma_f32_16x16x32_bf16 v[22:25], v[22:25], v[74:77], v[70:73]
	v_cndmask_b32_e64 v58, 0, v170, s[6:7]
	s_mov_b32 s6, m0
	s_mov_b32 m0, s68
	s_nop 0
	global_load_lds_dwordx4 v58, s[52:53]
	s_mov_b32 m0, s6
	ds_read_b64_tr_b16 v[58:59], v185 offset:16384
	ds_read_b64_tr_b16 v[60:61], v185 offset:17408
	s_waitcnt lgkmcnt(2)
	v_mfma_f32_16x16x32_bf16 v[30:33], v[54:57], v[74:77], v[30:33]
	ds_read_b64_tr_b16 v[54:55], v171 offset:24576
	ds_read_b64_tr_b16 v[56:57], v171 offset:25600
	ds_read_b128 v[66:69], v187
	s_waitcnt lgkmcnt(3)
	v_mfma_f32_16x16x32_bf16 v[10:13], v[58:61], v[74:77], v[10:13]
	ds_read_b64_tr_b16 v[58:59], v179 offset:24576
	ds_read_b64_tr_b16 v[60:61], v179 offset:25600
	s_waitcnt lgkmcnt(2)
	v_mfma_f32_16x16x32_bf16 v[94:97], v[54:57], v[66:69], v[42:45]
	s_nop 2
	ds_read_b64_tr_b16 v[42:43], v180 offset:24576
	ds_read_b64_tr_b16 v[44:45], v180 offset:25600
	s_waitcnt lgkmcnt(2)
	v_mfma_f32_16x16x32_bf16 v[90:93], v[58:61], v[66:69], v[50:53]
	s_nop 2
	ds_read_b64_tr_b16 v[50:51], v181 offset:24576
	ds_read_b64_tr_b16 v[52:53], v181 offset:25600
	s_waitcnt lgkmcnt(2)
	v_mfma_f32_16x16x32_bf16 v[70:73], v[42:45], v[66:69], v[38:41]
	s_nop 2
	ds_read_b64_tr_b16 v[38:39], v182 offset:24576
	ds_read_b64_tr_b16 v[40:41], v182 offset:25600
	s_waitcnt lgkmcnt(2)
	v_mfma_f32_16x16x32_bf16 v[42:45], v[50:53], v[66:69], v[26:29]
	s_nop 2
	ds_read_b64_tr_b16 v[26:27], v183 offset:24576
	ds_read_b64_tr_b16 v[28:29], v183 offset:25600
	s_waitcnt lgkmcnt(2)
	v_mfma_f32_16x16x32_bf16 v[86:89], v[38:41], v[66:69], v[34:37]
	s_cbranch_vccz .Lmy_tl_283_0
	global_load_dwordx4 v[38:41], v49, s[10:11]
.Lmy_tl_283_0:
	s_nop 2
	ds_read_b64_tr_b16 v[34:35], v184 offset:24576
	ds_read_b64_tr_b16 v[36:37], v184 offset:25600
	s_waitcnt lgkmcnt(2)
	v_mfma_f32_16x16x32_bf16 v[62:65], v[26:29], v[66:69], v[22:25]
	s_cbranch_vccz .Lmy_tl_283_1
	global_load_dwordx4 v[26:29], v49, s[10:11] offset:2048
.Lmy_tl_283_1:
	ds_read_b64_tr_b16 v[50:51], v185 offset:24576
	ds_read_b64_tr_b16 v[52:53], v185 offset:25600
	s_waitcnt lgkmcnt(2)
	v_mfma_f32_16x16x32_bf16 v[30:33], v[34:37], v[66:69], v[30:33]
	s_add_u32 s6, s69, 0x81000
	s_addc_u32 s7, s70, 0
	s_cbranch_vccz .Lmy_tl_283_2
	global_load_dwordx4 v[34:37], v49, s[6:7]
.Lmy_tl_283_2:
	s_waitcnt lgkmcnt(0)
	v_mfma_f32_16x16x32_bf16 v[10:13], v[50:53], v[66:69], v[10:13]
	s_cbranch_vccz .Lmy_tl_283_3
	global_load_dwordx4 v[22:25], v49, s[6:7] offset:2048
.Lmy_tl_283_3:
	s_waitcnt lgkmcnt(0)
	s_barrier
	s_mov_b32 s50, s51
	s_cbranch_vccnz .LBB0_283
	s_waitcnt vmcnt(0)
	s_waitcnt lgkmcnt(0)
	s_barrier
	v_mov_b32_e32 v77, 0
	v_mov_b32_e32 v76, v77
	v_mov_b32_e32 v75, v77
	v_mov_b32_e32 v74, v77
	v_mov_b32_e32 v81, v77
	v_mov_b32_e32 v80, v77
	v_mov_b32_e32 v79, v77
	v_mov_b32_e32 v78, v77
	v_mov_b32_e32 v125, v77
	v_mov_b32_e32 v124, v77
	v_mov_b32_e32 v123, v77
	v_mov_b32_e32 v122, v77
	v_mov_b32_e32 v49, v77
	v_mov_b32_e32 v48, v77
	v_mov_b32_e32 v47, v77
	v_mov_b32_e32 v46, v77
	v_mov_b32_e32 v61, v77
	v_mov_b32_e32 v60, v77
	v_mov_b32_e32 v59, v77
	v_mov_b32_e32 v58, v77
	v_mov_b32_e32 v117, v77
	v_mov_b32_e32 v116, v77
	v_mov_b32_e32 v115, v77
	v_mov_b32_e32 v114, v77
	v_mov_b32_e32 v21, v77
	v_mov_b32_e32 v20, v77
	v_mov_b32_e32 v19, v77
	v_mov_b32_e32 v18, v77
	v_mov_b32_e32 v41, v77
	v_mov_b32_e32 v40, v77
	v_mov_b32_e32 v39, v77
	v_mov_b32_e32 v38, v77
	v_mov_b32_e32 v109, v77
	v_mov_b32_e32 v108, v77
	v_mov_b32_e32 v107, v77
	v_mov_b32_e32 v106, v77
	v_mov_b32_e32 v9, v77
	v_mov_b32_e32 v8, v77
	v_mov_b32_e32 v7, v77
	v_mov_b32_e32 v6, v77
	v_mov_b32_e32 v25, v77
	v_mov_b32_e32 v24, v77
	v_mov_b32_e32 v23, v77
	v_mov_b32_e32 v22, v77
	v_mov_b32_e32 v105, v77
	v_mov_b32_e32 v104, v77
	v_mov_b32_e32 v103, v77
	v_mov_b32_e32 v102, v77
	v_mov_b32_e32 v57, v77
	v_mov_b32_e32 v56, v77
	v_mov_b32_e32 v55, v77
	v_mov_b32_e32 v54, v77
	v_mov_b32_e32 v85, v77
	v_mov_b32_e32 v84, v77
	v_mov_b32_e32 v83, v77
	v_mov_b32_e32 v82, v77
	v_mov_b32_e32 v129, v77
	v_mov_b32_e32 v128, v77
	v_mov_b32_e32 v127, v77
	v_mov_b32_e32 v126, v77
	v_mov_b32_e32 v37, v77
	v_mov_b32_e32 v36, v77
	v_mov_b32_e32 v35, v77
	v_mov_b32_e32 v34, v77
	v_mov_b32_e32 v69, v77
	v_mov_b32_e32 v68, v77
	v_mov_b32_e32 v67, v77
	v_mov_b32_e32 v66, v77
	v_mov_b32_e32 v121, v77
	v_mov_b32_e32 v120, v77
	v_mov_b32_e32 v119, v77
	v_mov_b32_e32 v118, v77
	v_mov_b32_e32 v17, v77
	v_mov_b32_e32 v16, v77
	v_mov_b32_e32 v15, v77
	v_mov_b32_e32 v14, v77
	v_mov_b32_e32 v53, v77
	v_mov_b32_e32 v52, v77
	v_mov_b32_e32 v51, v77
	v_mov_b32_e32 v50, v77
	v_mov_b32_e32 v113, v77
	v_mov_b32_e32 v112, v77
	v_mov_b32_e32 v111, v77
	v_mov_b32_e32 v110, v77
	v_mov_b32_e32 v5, v77
	v_mov_b32_e32 v4, v77
	v_mov_b32_e32 v3, v77
	v_mov_b32_e32 v2, v77
	v_mov_b32_e32 v29, v77
	v_mov_b32_e32 v28, v77
	v_mov_b32_e32 v27, v77
	v_mov_b32_e32 v26, v77
	v_mov_b32_e32 v101, v77
	v_mov_b32_e32 v100, v77
	v_mov_b32_e32 v99, v77
	v_mov_b32_e32 v98, v77

.LBB0_873:
	s_waitcnt vmcnt(4)
	s_min_u32 s10, s48, 12
	ds_read_b128 v[148:151], v172
	ds_read_b128 v[152:155], v172 offset:2048
	ds_read_b128 v[156:159], v172 offset:4096
	ds_read_b64_tr_b16 v[178:179], v171
	ds_read_b64_tr_b16 v[180:181], v171 offset:1024
	s_cmp_lt_u32 s48, 13
	s_cselect_b64 vcc, -1, 0
	s_lshl_b32 s10, s10, 17
	s_add_u32 s49, s22, s10
	s_addc_u32 s77, s23, 0
	s_add_u32 s10, s49, 0x60000
	ds_read_b64_tr_b16 v[182:183], v141
	ds_read_b64_tr_b16 v[184:185], v141 offset:1024
	s_addc_u32 s11, s77, 0
	s_waitcnt lgkmcnt(2)
	v_mfma_f32_16x16x32_bf16 v[94:97], v[178:181], v[148:151], v[94:97]
	s_add_u32 s46, s8, s14
	s_addc_u32 s47, s9, s15
	s_add_u32 s46, s46, 0x80
	v_mfma_f32_16x16x32_bf16 v[74:77], v[178:181], v[152:155], v[74:77]
	v_cvt_pk_bf16_f32 v106, v106, v107
	v_cvt_pk_bf16_f32 v107, v108, v109
	v_cndmask_b32_e32 v160, 0, v168, vcc
	v_mfma_f32_16x16x32_bf16 v[78:81], v[178:181], v[156:159], v[78:81]
	s_addc_u32 s47, s47, 0
	ds_write_b64 v135, v[106:107] offset:16384
	ds_read_b64_tr_b16 v[106:107], v142
	ds_read_b64_tr_b16 v[108:109], v142 offset:1024
	s_waitcnt lgkmcnt(3)
	v_mfma_f32_16x16x32_bf16 v[90:93], v[182:185], v[148:151], v[90:93]
	v_cvt_pk_bf16_f32 v102, v102, v103
	v_cvt_pk_bf16_f32 v103, v104, v105
	ds_write_b64 v136, v[102:103] offset:16640
	v_mfma_f32_16x16x32_bf16 v[46:49], v[182:185], v[152:155], v[46:49]
	v_mfma_f32_16x16x32_bf16 v[58:61], v[182:185], v[156:159], v[58:61]
	ds_read_b64_tr_b16 v[102:103], v143
	ds_read_b64_tr_b16 v[104:105], v143 offset:1024
	s_waitcnt lgkmcnt(3)
	v_mfma_f32_16x16x32_bf16 v[70:73], v[106:109], v[148:151], v[70:73]
	v_cvt_pk_bf16_f32 v110, v110, v111
	v_cvt_pk_bf16_f32 v111, v112, v113
	ds_write_b64 v137, v[110:111] offset:16896
	v_mfma_f32_16x16x32_bf16 v[18:21], v[106:109], v[152:155], v[18:21]
	v_mfma_f32_16x16x32_bf16 v[38:41], v[106:109], v[156:159], v[38:41]
	ds_read_b64_tr_b16 v[106:107], v144
	ds_read_b64_tr_b16 v[108:109], v144 offset:1024
	s_waitcnt lgkmcnt(3)
	v_mfma_f32_16x16x32_bf16 v[42:45], v[102:105], v[148:151], v[42:45]
	v_cvt_pk_bf16_f32 v98, v98, v99
	v_cvt_pk_bf16_f32 v99, v100, v101
	ds_write_b64 v138, v[98:99] offset:17152
	v_mfma_f32_16x16x32_bf16 v[6:9], v[102:105], v[152:155], v[6:9]
	v_mfma_f32_16x16x32_bf16 v[22:25], v[102:105], v[156:159], v[22:25]
	ds_read_b64_tr_b16 v[98:99], v145
	ds_read_b64_tr_b16 v[100:101], v145 offset:1024
	s_waitcnt lgkmcnt(3)
	v_mfma_f32_16x16x32_bf16 v[86:89], v[106:109], v[148:151], v[86:89]
	s_mov_b32 s78, m0
	s_mov_b32 m0, s71
	s_nop 0
	global_load_lds_dwordx4 v169, s[46:47]
	s_mov_b32 m0, s78
	v_mfma_f32_16x16x32_bf16 v[54:57], v[106:109], v[152:155], v[54:57]
	v_mfma_f32_16x16x32_bf16 v[82:85], v[106:109], v[156:159], v[82:85]
	ds_read_b64_tr_b16 v[102:103], v146
	ds_read_b64_tr_b16 v[104:105], v146 offset:1024
	s_waitcnt lgkmcnt(2)
	v_mfma_f32_16x16x32_bf16 v[62:65], v[98:101], v[148:151], v[62:65]
	s_mov_b32 s78, m0
	s_mov_b32 m0, s72
	s_nop 0
	global_load_lds_dwordx4 v170, s[46:47]
	s_mov_b32 m0, s78
	v_mfma_f32_16x16x32_bf16 v[34:37], v[98:101], v[152:155], v[34:37]
	v_mfma_f32_16x16x32_bf16 v[66:69], v[98:101], v[156:159], v[66:69]
	ds_read_b64_tr_b16 v[98:99], v147
	ds_read_b64_tr_b16 v[100:101], v147 offset:1024
	s_waitcnt lgkmcnt(2)
	v_mfma_f32_16x16x32_bf16 v[30:33], v[102:105], v[148:151], v[30:33]
	s_mov_b32 s78, m0
	s_mov_b32 m0, s73
	s_nop 0
	global_load_lds_dwordx4 v174, s[46:47]
	s_mov_b32 m0, s78
	v_mfma_f32_16x16x32_bf16 v[14:17], v[102:105], v[152:155], v[14:17]
	v_mfma_f32_16x16x32_bf16 v[50:53], v[102:105], v[156:159], v[50:53]
	s_waitcnt lgkmcnt(0)
	v_mfma_f32_16x16x32_bf16 v[10:13], v[98:101], v[148:151], v[10:13]
	ds_read_b64_tr_b16 v[102:103], v171 offset:8192
	ds_read_b64_tr_b16 v[104:105], v171 offset:9216
	v_mfma_f32_16x16x32_bf16 v[2:5], v[98:101], v[152:155], v[2:5]
	ds_read_b128 v[148:151], v139
	ds_read_b128 v[152:155], v139 offset:2048
	ds_read_b128 v[178:181], v139 offset:4096
	s_mov_b32 s78, m0
	s_mov_b32 m0, s74
	s_nop 0
	global_load_lds_dwordx4 v175, s[46:47]
	s_mov_b32 m0, s78
	v_mfma_f32_16x16x32_bf16 v[26:29], v[98:101], v[156:159], v[26:29]
	ds_read_b64_tr_b16 v[98:99], v141 offset:8192
	ds_read_b64_tr_b16 v[100:101], v141 offset:9216
	s_waitcnt lgkmcnt(4)
	v_mfma_f32_16x16x32_bf16 v[94:97], v[102:105], v[148:151], v[94:97]
	s_mov_b32 s78, m0
	s_mov_b32 m0, s75
	s_nop 0
	global_load_lds_dwordx4 v176, s[46:47]
	s_mov_b32 m0, s78
	s_waitcnt lgkmcnt(3)
	v_mfma_f32_16x16x32_bf16 v[74:77], v[102:105], v[152:155], v[74:77]
	s_waitcnt lgkmcnt(2)
	v_mfma_f32_16x16x32_bf16 v[78:81], v[102:105], v[178:181], v[78:81]
	ds_read_b64_tr_b16 v[102:103], v142 offset:8192
	ds_read_b64_tr_b16 v[104:105], v142 offset:9216
	s_waitcnt lgkmcnt(2)
	v_mfma_f32_16x16x32_bf16 v[90:93], v[98:101], v[148:151], v[90:93]
	s_mov_b32 s78, m0
	s_mov_b32 m0, s76
	s_nop 0
	global_load_lds_dwordx4 v177, s[46:47]
	s_mov_b32 m0, s78
	v_mfma_f32_16x16x32_bf16 v[46:49], v[98:101], v[152:155], v[46:49]
	v_mfma_f32_16x16x32_bf16 v[58:61], v[98:101], v[178:181], v[58:61]
	ds_read_b64_tr_b16 v[98:99], v143 offset:8192
	ds_read_b64_tr_b16 v[100:101], v143 offset:9216
	s_waitcnt lgkmcnt(2)
	v_mfma_f32_16x16x32_bf16 v[70:73], v[102:105], v[148:151], v[70:73]
	v_mfma_f32_16x16x32_bf16 v[18:21], v[102:105], v[152:155], v[18:21]
	v_mfma_f32_16x16x32_bf16 v[38:41], v[102:105], v[178:181], v[38:41]
	ds_read_b64_tr_b16 v[102:103], v144 offset:8192
	ds_read_b64_tr_b16 v[104:105], v144 offset:9216
	s_waitcnt lgkmcnt(2)
	v_mfma_f32_16x16x32_bf16 v[42:45], v[98:101], v[148:151], v[42:45]
	v_mfma_f32_16x16x32_bf16 v[6:9], v[98:101], v[152:155], v[6:9]
	v_mfma_f32_16x16x32_bf16 v[22:25], v[98:101], v[178:181], v[22:25]
	ds_read_b64_tr_b16 v[98:99], v145 offset:8192
	ds_read_b64_tr_b16 v[100:101], v145 offset:9216
	s_waitcnt lgkmcnt(2)
	v_mfma_f32_16x16x32_bf16 v[86:89], v[102:105], v[148:151], v[86:89]
	global_load_dwordx4 v[106:109], v160, s[10:11]
	v_mfma_f32_16x16x32_bf16 v[54:57], v[102:105], v[152:155], v[54:57]
	v_mfma_f32_16x16x32_bf16 v[82:85], v[102:105], v[178:181], v[82:85]
	ds_read_b64_tr_b16 v[156:157], v146 offset:8192
	ds_read_b64_tr_b16 v[158:159], v146 offset:9216
	s_waitcnt lgkmcnt(2)
	v_mfma_f32_16x16x32_bf16 v[62:65], v[98:101], v[148:151], v[62:65]
	global_load_dwordx4 v[102:105], v160, s[10:11] offset:2048
	v_mfma_f32_16x16x32_bf16 v[34:37], v[98:101], v[152:155], v[34:37]
	v_mfma_f32_16x16x32_bf16 v[66:69], v[98:101], v[178:181], v[66:69]
	ds_read_b64_tr_b16 v[182:183], v147 offset:8192
	ds_read_b64_tr_b16 v[184:185], v147 offset:9216
	s_waitcnt lgkmcnt(2)
	v_mfma_f32_16x16x32_bf16 v[30:33], v[156:159], v[148:151], v[30:33]
	s_add_u32 s10, s49, 0x61000
	s_addc_u32 s11, s77, 0
	global_load_dwordx4 v[110:113], v160, s[10:11]
	v_mfma_f32_16x16x32_bf16 v[14:17], v[156:159], v[152:155], v[14:17]
	v_mfma_f32_16x16x32_bf16 v[50:53], v[156:159], v[178:181], v[50:53]
	s_waitcnt lgkmcnt(0)
	v_mfma_f32_16x16x32_bf16 v[10:13], v[182:185], v[148:151], v[10:13]
	global_load_dwordx4 v[98:101], v160, s[10:11] offset:2048
	v_mfma_f32_16x16x32_bf16 v[2:5], v[182:185], v[152:155], v[2:5]
	v_mfma_f32_16x16x32_bf16 v[26:29], v[182:185], v[178:181], v[26:29]
	s_min_u32 s10, s48, 11
	s_add_i32 s77, s48, 2
	s_cmp_lt_u32 s48, 12
	s_cselect_b64 vcc, -1, 0
	s_lshl_b32 s10, s10, 17
	s_waitcnt lgkmcnt(0)
	s_barrier
	s_add_u32 s78, s22, s10
	s_waitcnt vmcnt(4)
	s_addc_u32 s80, s23, 0
	s_add_u32 s46, s78, 0x80000
	ds_read_b64_tr_b16 v[148:149], v171 offset:16384
	ds_read_b64_tr_b16 v[150:151], v171 offset:17408
	ds_read_b128 v[152:155], v172 offset:8192
	ds_read_b128 v[156:159], v172 offset:10240
	ds_read_b128 v[178:181], v172 offset:12288
	s_addc_u32 s47, s80, 0
	s_add_u32 s14, s14, 0x100
	s_addc_u32 s15, s15, 0
	s_cmp_lt_u32 s48, 14
	ds_read_b64_tr_b16 v[182:183], v141 offset:16384
	ds_read_b64_tr_b16 v[184:185], v141 offset:17408
	s_cselect_b64 s[10:11], -1, 0
	s_waitcnt lgkmcnt(4)
	v_mfma_f32_16x16x32_bf16 v[94:97], v[148:151], v[152:155], v[94:97]
	v_cndmask_b32_e32 v160, 0, v168, vcc
	s_and_b64 vcc, s[10:11], exec
	s_cselect_b32 s48, s14, 0x780
	s_waitcnt lgkmcnt(3)
	v_mfma_f32_16x16x32_bf16 v[74:77], v[148:151], v[156:159], v[74:77]
	s_add_u32 s48, s8, s48
	v_cvt_pk_bf16_f32 v122, v122, v123
	v_cvt_pk_bf16_f32 v123, v124, v125
	s_waitcnt lgkmcnt(2)
	v_mfma_f32_16x16x32_bf16 v[78:81], v[148:151], v[178:181], v[78:81]
	s_addc_u32 s49, s9, 0
	ds_write_b64 v135, v[122:123]
	ds_read_b64_tr_b16 v[122:123], v142 offset:16384
	ds_read_b64_tr_b16 v[124:125], v142 offset:17408
	s_waitcnt lgkmcnt(3)
	v_mfma_f32_16x16x32_bf16 v[90:93], v[182:185], v[152:155], v[90:93]
	v_cvt_pk_bf16_f32 v118, v118, v119
	v_cvt_pk_bf16_f32 v119, v120, v121
	ds_write_b64 v136, v[118:119] offset:256
	v_mfma_f32_16x16x32_bf16 v[46:49], v[182:185], v[156:159], v[46:49]
	v_mfma_f32_16x16x32_bf16 v[58:61], v[182:185], v[178:181], v[58:61]
	ds_read_b64_tr_b16 v[118:119], v143 offset:16384
	ds_read_b64_tr_b16 v[120:121], v143 offset:17408
	s_waitcnt lgkmcnt(3)
	v_mfma_f32_16x16x32_bf16 v[70:73], v[122:125], v[152:155], v[70:73]
	v_cvt_pk_bf16_f32 v126, v126, v127
	v_cvt_pk_bf16_f32 v127, v128, v129
	ds_write_b64 v137, v[126:127] offset:512
	v_mfma_f32_16x16x32_bf16 v[18:21], v[122:125], v[156:159], v[18:21]
	v_mfma_f32_16x16x32_bf16 v[38:41], v[122:125], v[178:181], v[38:41]
	ds_read_b64_tr_b16 v[122:123], v144 offset:16384
	ds_read_b64_tr_b16 v[124:125], v144 offset:17408
	s_waitcnt lgkmcnt(3)
	v_mfma_f32_16x16x32_bf16 v[42:45], v[118:121], v[152:155], v[42:45]
	v_cvt_pk_bf16_f32 v114, v114, v115
	v_cvt_pk_bf16_f32 v115, v116, v117
	ds_write_b64 v138, v[114:115] offset:768
	v_mfma_f32_16x16x32_bf16 v[6:9], v[118:121], v[156:159], v[6:9]
	v_mfma_f32_16x16x32_bf16 v[22:25], v[118:121], v[178:181], v[22:25]
	ds_read_b64_tr_b16 v[114:115], v145 offset:16384
	ds_read_b64_tr_b16 v[116:117], v145 offset:17408
	s_waitcnt lgkmcnt(3)
	v_mfma_f32_16x16x32_bf16 v[86:89], v[122:125], v[152:155], v[86:89]
	v_cndmask_b32_e64 v118, 0, v169, s[10:11]
	s_mov_b32 s81, m0
	s_mov_b32 m0, s67
	s_nop 0
	global_load_lds_dwordx4 v118, s[48:49]
	s_mov_b32 m0, s81
	v_mfma_f32_16x16x32_bf16 v[54:57], v[122:125], v[156:159], v[54:57]
	v_mfma_f32_16x16x32_bf16 v[82:85], v[122:125], v[178:181], v[82:85]
	ds_read_b64_tr_b16 v[118:119], v146 offset:16384
	ds_read_b64_tr_b16 v[120:121], v146 offset:17408
	s_waitcnt lgkmcnt(2)
	v_mfma_f32_16x16x32_bf16 v[62:65], v[114:117], v[152:155], v[62:65]
	v_cndmask_b32_e64 v122, 0, v170, s[10:11]
	s_mov_b32 s81, m0
	s_mov_b32 m0, s68
	s_nop 0
	global_load_lds_dwordx4 v122, s[48:49]
	s_mov_b32 m0, s81
	v_mfma_f32_16x16x32_bf16 v[34:37], v[114:117], v[156:159], v[34:37]
	v_mfma_f32_16x16x32_bf16 v[66:69], v[114:117], v[178:181], v[66:69]
	ds_read_b64_tr_b16 v[114:115], v147 offset:16384
	ds_read_b64_tr_b16 v[116:117], v147 offset:17408
	s_waitcnt lgkmcnt(2)
	v_mfma_f32_16x16x32_bf16 v[30:33], v[118:121], v[152:155], v[30:33]
	v_cndmask_b32_e64 v122, 0, v174, s[10:11]
	s_mov_b32 s81, m0
	s_mov_b32 m0, s50
	s_nop 0
	global_load_lds_dwordx4 v122, s[48:49]
	s_mov_b32 m0, s81
	v_mfma_f32_16x16x32_bf16 v[14:17], v[118:121], v[156:159], v[14:17]
	v_mfma_f32_16x16x32_bf16 v[50:53], v[118:121], v[178:181], v[50:53]
	s_waitcnt lgkmcnt(0)
	v_mfma_f32_16x16x32_bf16 v[10:13], v[114:117], v[152:155], v[10:13]
	ds_read_b64_tr_b16 v[118:119], v171 offset:24576
	ds_read_b64_tr_b16 v[120:121], v171 offset:25600
	v_cndmask_b32_e64 v122, 0, v175, s[10:11]
	v_mfma_f32_16x16x32_bf16 v[2:5], v[114:117], v[156:159], v[2:5]
	ds_read_b128 v[148:151], v140
	ds_read_b128 v[152:155], v140 offset:2048
	ds_read_b128 v[156:159], v140 offset:4096
	s_mov_b32 s81, m0
	s_mov_b32 m0, s51
	s_nop 0
	global_load_lds_dwordx4 v122, s[48:49]
	s_mov_b32 m0, s81
	v_mfma_f32_16x16x32_bf16 v[26:29], v[114:117], v[178:181], v[26:29]
	ds_read_b64_tr_b16 v[114:115], v141 offset:24576
	ds_read_b64_tr_b16 v[116:117], v141 offset:25600
	s_waitcnt lgkmcnt(4)
	v_mfma_f32_16x16x32_bf16 v[94:97], v[118:121], v[148:151], v[94:97]
	v_cndmask_b32_e64 v122, 0, v176, s[10:11]
	s_mov_b32 s81, m0
	s_mov_b32 m0, s69
	s_nop 0
	global_load_lds_dwordx4 v122, s[48:49]
	s_mov_b32 m0, s81
	s_waitcnt lgkmcnt(3)
	v_mfma_f32_16x16x32_bf16 v[74:77], v[118:121], v[152:155], v[74:77]
	s_waitcnt lgkmcnt(2)
	v_mfma_f32_16x16x32_bf16 v[78:81], v[118:121], v[156:159], v[78:81]
	ds_read_b64_tr_b16 v[118:119], v142 offset:24576
	ds_read_b64_tr_b16 v[120:121], v142 offset:25600
	s_waitcnt lgkmcnt(2)
	v_mfma_f32_16x16x32_bf16 v[90:93], v[114:117], v[148:151], v[90:93]
	v_cndmask_b32_e64 v122, 0, v177, s[10:11]
	s_mov_b32 s10, m0
	s_mov_b32 m0, s70
	s_nop 0
	global_load_lds_dwordx4 v122, s[48:49]
	s_mov_b32 m0, s10
	v_mfma_f32_16x16x32_bf16 v[46:49], v[114:117], v[152:155], v[46:49]
	v_mfma_f32_16x16x32_bf16 v[58:61], v[114:117], v[156:159], v[58:61]
	ds_read_b64_tr_b16 v[114:115], v143 offset:24576
	ds_read_b64_tr_b16 v[116:117], v143 offset:25600
	s_waitcnt lgkmcnt(2)
	v_mfma_f32_16x16x32_bf16 v[70:73], v[118:121], v[148:151], v[70:73]
	v_mfma_f32_16x16x32_bf16 v[18:21], v[118:121], v[152:155], v[18:21]
	v_mfma_f32_16x16x32_bf16 v[38:41], v[118:121], v[156:159], v[38:41]
	ds_read_b64_tr_b16 v[118:119], v144 offset:24576
	ds_read_b64_tr_b16 v[120:121], v144 offset:25600
	s_waitcnt lgkmcnt(2)
	v_mfma_f32_16x16x32_bf16 v[42:45], v[114:117], v[148:151], v[42:45]
	v_mfma_f32_16x16x32_bf16 v[6:9], v[114:117], v[152:155], v[6:9]
	v_mfma_f32_16x16x32_bf16 v[22:25], v[114:117], v[156:159], v[22:25]
	ds_read_b64_tr_b16 v[114:115], v145 offset:24576
	ds_read_b64_tr_b16 v[116:117], v145 offset:25600
	s_waitcnt lgkmcnt(2)
	v_mfma_f32_16x16x32_bf16 v[86:89], v[118:121], v[148:151], v[86:89]
	s_cbranch_vccz .Lmy_tl_873_0
	global_load_dwordx4 v[122:125], v160, s[46:47]
.Lmy_tl_873_0:
	v_mfma_f32_16x16x32_bf16 v[54:57], v[118:121], v[152:155], v[54:57]
	v_mfma_f32_16x16x32_bf16 v[82:85], v[118:121], v[156:159], v[82:85]
	ds_read_b64_tr_b16 v[178:179], v146 offset:24576
	ds_read_b64_tr_b16 v[180:181], v146 offset:25600
	s_waitcnt lgkmcnt(2)
	v_mfma_f32_16x16x32_bf16 v[62:65], v[114:117], v[148:151], v[62:65]
	s_cbranch_vccz .Lmy_tl_873_1
	global_load_dwordx4 v[118:121], v160, s[46:47] offset:2048
.Lmy_tl_873_1:
	v_mfma_f32_16x16x32_bf16 v[34:37], v[114:117], v[152:155], v[34:37]
	v_mfma_f32_16x16x32_bf16 v[66:69], v[114:117], v[156:159], v[66:69]
	ds_read_b64_tr_b16 v[182:183], v147 offset:24576
	ds_read_b64_tr_b16 v[184:185], v147 offset:25600
	s_waitcnt lgkmcnt(2)
	v_mfma_f32_16x16x32_bf16 v[30:33], v[178:181], v[148:151], v[30:33]
	s_add_u32 s10, s78, 0x81000
	s_addc_u32 s11, s80, 0
	s_cbranch_vccz .Lmy_tl_873_2
	global_load_dwordx4 v[126:129], v160, s[10:11]
.Lmy_tl_873_2:
	v_mfma_f32_16x16x32_bf16 v[14:17], v[178:181], v[152:155], v[14:17]
	v_mfma_f32_16x16x32_bf16 v[50:53], v[178:181], v[156:159], v[50:53]
	s_waitcnt lgkmcnt(0)
	v_mfma_f32_16x16x32_bf16 v[10:13], v[182:185], v[148:151], v[10:13]
	s_cbranch_vccz .Lmy_tl_873_3
	global_load_dwordx4 v[114:117], v160, s[10:11] offset:2048
.Lmy_tl_873_3:
	v_mfma_f32_16x16x32_bf16 v[2:5], v[182:185], v[152:155], v[2:5]
	v_mfma_f32_16x16x32_bf16 v[26:29], v[182:185], v[156:159], v[26:29]
	s_waitcnt lgkmcnt(0)
	s_barrier
	s_mov_b32 s48, s77
	s_cbranch_vccnz .LBB0_873
	s_waitcnt vmcnt(0)
	s_waitcnt lgkmcnt(0)
	s_barrier
	s_mov_b64 s[14:15], 0
	s_branch .LBB0_880

.LBB0_878:
	s_waitcnt vmcnt(4)
	s_min_u32 s10, s50, 12
	ds_read_b128 v[112:115], v172
	ds_read_b128 v[116:119], v172 offset:2048
	s_cmp_lt_u32 s50, 13
	ds_read_b64_tr_b16 v[120:121], v171
	ds_read_b64_tr_b16 v[122:123], v171 offset:1024
	s_cselect_b64 vcc, -1, 0
	s_lshl_b32 s10, s10, 17
	s_add_u32 s51, s22, s10
	s_addc_u32 s75, s23, 0
	s_add_u32 s10, s51, 0x60000
	ds_read_b64_tr_b16 v[124:125], v104
	ds_read_b64_tr_b16 v[126:127], v104 offset:1024
	s_addc_u32 s11, s75, 0
	s_waitcnt lgkmcnt(2)
	v_mfma_f32_16x16x32_bf16 v[94:97], v[120:123], v[112:115], v[94:97]
	s_add_u32 s48, s8, s46
	s_addc_u32 s49, s9, s47
	s_add_u32 s48, s48, 0x80
	v_mfma_f32_16x16x32_bf16 v[74:77], v[120:123], v[116:119], v[74:77]
	v_cvt_pk_bf16_f32 v38, v38, v39
	v_cvt_pk_bf16_f32 v39, v40, v41
	v_cndmask_b32_e32 v111, 0, v168, vcc
	s_addc_u32 s49, s49, 0
	ds_write_b64 v98, v[38:39] offset:16384
	ds_read_b64_tr_b16 v[38:39], v105
	ds_read_b64_tr_b16 v[40:41], v105 offset:1024
	v_cvt_pk_bf16_f32 v26, v26, v27
	v_cvt_pk_bf16_f32 v27, v28, v29
	s_waitcnt lgkmcnt(3)
	v_mfma_f32_16x16x32_bf16 v[90:93], v[124:127], v[112:115], v[90:93]
	ds_write_b64 v99, v[26:27] offset:16640
	v_mfma_f32_16x16x32_bf16 v[26:29], v[124:127], v[116:119], v[46:49]
	s_nop 2
	ds_read_b64_tr_b16 v[46:47], v106
	ds_read_b64_tr_b16 v[48:49], v106 offset:1024
	s_waitcnt lgkmcnt(3)
	v_mfma_f32_16x16x32_bf16 v[70:73], v[38:41], v[112:115], v[70:73]
	v_cvt_pk_bf16_f32 v50, v50, v51
	v_cvt_pk_bf16_f32 v51, v52, v53
	ds_write_b64 v100, v[50:51] offset:16896
	v_mfma_f32_16x16x32_bf16 v[18:21], v[38:41], v[116:119], v[18:21]
	ds_read_b64_tr_b16 v[38:39], v107
	ds_read_b64_tr_b16 v[40:41], v107 offset:1024
	s_waitcnt lgkmcnt(3)
	v_mfma_f32_16x16x32_bf16 v[42:45], v[46:49], v[112:115], v[42:45]
	v_cvt_pk_bf16_f32 v22, v22, v23
	v_cvt_pk_bf16_f32 v23, v24, v25
	ds_write_b64 v101, v[22:23] offset:17152
	v_mfma_f32_16x16x32_bf16 v[6:9], v[46:49], v[116:119], v[6:9]
	ds_read_b64_tr_b16 v[46:47], v108
	ds_read_b64_tr_b16 v[48:49], v108 offset:1024
	s_waitcnt lgkmcnt(3)
	v_mfma_f32_16x16x32_bf16 v[22:25], v[38:41], v[112:115], v[86:89]
	s_mov_b32 s76, m0
	s_mov_b32 m0, s71
	s_nop 0
	global_load_lds_dwordx4 v169, s[48:49]
	s_mov_b32 m0, s76
	v_mfma_f32_16x16x32_bf16 v[50:53], v[38:41], v[116:119], v[54:57]
	ds_read_b64_tr_b16 v[38:39], v109
	ds_read_b64_tr_b16 v[40:41], v109 offset:1024
	s_waitcnt lgkmcnt(2)
	v_mfma_f32_16x16x32_bf16 v[54:57], v[46:49], v[112:115], v[62:65]
	s_mov_b32 s76, m0
	s_mov_b32 m0, s72
	s_nop 0
	global_load_lds_dwordx4 v170, s[48:49]
	s_mov_b32 m0, s76
	v_mfma_f32_16x16x32_bf16 v[34:37], v[46:49], v[116:119], v[34:37]
	ds_read_b64_tr_b16 v[46:47], v110
	ds_read_b64_tr_b16 v[48:49], v110 offset:1024
	s_waitcnt lgkmcnt(2)
	v_mfma_f32_16x16x32_bf16 v[30:33], v[38:41], v[112:115], v[30:33]
	s_mov_b32 s76, m0
	s_mov_b32 m0, s73
	s_nop 0
	global_load_lds_dwordx4 v174, s[48:49]
	s_mov_b32 m0, s76
	v_mfma_f32_16x16x32_bf16 v[14:17], v[38:41], v[116:119], v[14:17]
	ds_read_b64_tr_b16 v[38:39], v171 offset:8192
	ds_read_b64_tr_b16 v[40:41], v171 offset:9216
	ds_read_b128 v[62:65], v102
	ds_read_b128 v[86:89], v102 offset:2048
	s_waitcnt lgkmcnt(4)
	v_mfma_f32_16x16x32_bf16 v[10:13], v[46:49], v[112:115], v[10:13]
	s_mov_b32 s76, m0
	s_mov_b32 m0, s74
	s_nop 0
	global_load_lds_dwordx4 v175, s[48:49]
	s_mov_b32 m0, s76
	v_mfma_f32_16x16x32_bf16 v[2:5], v[46:49], v[116:119], v[2:5]
	s_waitcnt lgkmcnt(1)
	v_mfma_f32_16x16x32_bf16 v[46:49], v[38:41], v[62:65], v[94:97]
	s_nop 2
	ds_read_b64_tr_b16 v[94:95], v104 offset:8192
	ds_read_b64_tr_b16 v[96:97], v104 offset:9216
	s_waitcnt lgkmcnt(2)
	v_mfma_f32_16x16x32_bf16 v[74:77], v[38:41], v[86:89], v[74:77]
	ds_read_b64_tr_b16 v[38:39], v105 offset:8192
	ds_read_b64_tr_b16 v[40:41], v105 offset:9216
	s_waitcnt lgkmcnt(2)
	v_mfma_f32_16x16x32_bf16 v[90:93], v[94:97], v[62:65], v[90:93]
	v_mfma_f32_16x16x32_bf16 v[94:97], v[94:97], v[86:89], v[26:29]
	s_nop 2
	ds_read_b64_tr_b16 v[26:27], v106 offset:8192
	ds_read_b64_tr_b16 v[28:29], v106 offset:9216
	s_waitcnt lgkmcnt(2)
	v_mfma_f32_16x16x32_bf16 v[70:73], v[38:41], v[62:65], v[70:73]
	v_mfma_f32_16x16x32_bf16 v[18:21], v[38:41], v[86:89], v[18:21]
	ds_read_b64_tr_b16 v[112:113], v107 offset:8192
	ds_read_b64_tr_b16 v[114:115], v107 offset:9216
	s_waitcnt lgkmcnt(2)
	v_mfma_f32_16x16x32_bf16 v[42:45], v[26:29], v[62:65], v[42:45]
	v_mfma_f32_16x16x32_bf16 v[6:9], v[26:29], v[86:89], v[6:9]
	s_waitcnt lgkmcnt(0)
	v_mfma_f32_16x16x32_bf16 v[116:119], v[112:115], v[62:65], v[22:25]
	s_nop 2
	ds_read_b64_tr_b16 v[22:23], v108 offset:8192
	ds_read_b64_tr_b16 v[24:25], v108 offset:9216
	global_load_dwordx4 v[38:41], v111, s[10:11]
	v_mfma_f32_16x16x32_bf16 v[112:115], v[112:115], v[86:89], v[50:53]
	ds_read_b64_tr_b16 v[120:121], v109 offset:8192
	ds_read_b64_tr_b16 v[122:123], v109 offset:9216
	s_waitcnt lgkmcnt(2)
	v_mfma_f32_16x16x32_bf16 v[54:57], v[22:25], v[62:65], v[54:57]
	global_load_dwordx4 v[26:29], v111, s[10:11] offset:2048
	v_mfma_f32_16x16x32_bf16 v[34:37], v[22:25], v[86:89], v[34:37]
	ds_read_b64_tr_b16 v[124:125], v110 offset:8192
	ds_read_b64_tr_b16 v[126:127], v110 offset:9216
	s_waitcnt lgkmcnt(2)
	v_mfma_f32_16x16x32_bf16 v[30:33], v[120:123], v[62:65], v[30:33]
	s_add_u32 s10, s51, 0x61000
	s_addc_u32 s11, s75, 0
	global_load_dwordx4 v[50:53], v111, s[10:11]
	v_mfma_f32_16x16x32_bf16 v[14:17], v[120:123], v[86:89], v[14:17]
	s_waitcnt lgkmcnt(0)
	v_mfma_f32_16x16x32_bf16 v[10:13], v[124:127], v[62:65], v[10:13]
	global_load_dwordx4 v[22:25], v111, s[10:11] offset:2048
	v_mfma_f32_16x16x32_bf16 v[2:5], v[124:127], v[86:89], v[2:5]
	s_min_u32 s10, s50, 11
	s_add_i32 s75, s50, 2
	s_cmp_lt_u32 s50, 12
	s_cselect_b64 vcc, -1, 0
	s_lshl_b32 s10, s10, 17
	s_waitcnt lgkmcnt(0)
	s_barrier
	s_add_u32 s76, s22, s10
	s_waitcnt vmcnt(4)
	s_addc_u32 s77, s23, 0
	s_add_u32 s48, s76, 0x80000
	ds_read_b64_tr_b16 v[62:63], v171 offset:16384
	ds_read_b64_tr_b16 v[64:65], v171 offset:17408
	ds_read_b128 v[86:89], v172 offset:8192
	ds_read_b128 v[120:123], v172 offset:10240
	s_addc_u32 s49, s77, 0
	s_add_u32 s46, s46, 0x100
	s_addc_u32 s47, s47, 0
	s_cmp_lt_u32 s50, 14
	ds_read_b64_tr_b16 v[124:125], v104 offset:16384
	ds_read_b64_tr_b16 v[126:127], v104 offset:17408
	s_cselect_b64 s[10:11], -1, 0
	s_waitcnt lgkmcnt(3)
	v_mfma_f32_16x16x32_bf16 v[46:49], v[62:65], v[86:89], v[46:49]
	v_cndmask_b32_e32 v111, 0, v168, vcc
	s_and_b64 vcc, s[10:11], exec
	s_cselect_b32 s50, s46, 0x780
	s_waitcnt lgkmcnt(2)
	v_mfma_f32_16x16x32_bf16 v[62:65], v[62:65], v[120:123], v[74:77]
	s_add_u32 s50, s8, s50
	s_addc_u32 s51, s9, 0
	s_nop 0
	v_cvt_pk_bf16_f32 v74, v78, v79
	v_cvt_pk_bf16_f32 v75, v80, v81
	ds_write_b64 v98, v[74:75]
	ds_read_b64_tr_b16 v[74:75], v105 offset:16384
	ds_read_b64_tr_b16 v[76:77], v105 offset:17408
	v_cvt_pk_bf16_f32 v66, v66, v67
	v_cvt_pk_bf16_f32 v67, v68, v69
	s_waitcnt lgkmcnt(3)
	v_mfma_f32_16x16x32_bf16 v[78:81], v[124:127], v[86:89], v[90:93]
	ds_write_b64 v99, v[66:67] offset:256
	v_mfma_f32_16x16x32_bf16 v[66:69], v[124:127], v[120:123], v[94:97]
	s_nop 0
	ds_read_b64_tr_b16 v[90:91], v106 offset:16384
	ds_read_b64_tr_b16 v[92:93], v106 offset:17408
	s_waitcnt lgkmcnt(3)
	v_mfma_f32_16x16x32_bf16 v[70:73], v[74:77], v[86:89], v[70:73]
	v_cvt_pk_bf16_f32 v82, v82, v83
	v_cvt_pk_bf16_f32 v83, v84, v85
	ds_write_b64 v100, v[82:83] offset:512
	v_mfma_f32_16x16x32_bf16 v[18:21], v[74:77], v[120:123], v[18:21]
	ds_read_b64_tr_b16 v[74:75], v107 offset:16384
	ds_read_b64_tr_b16 v[76:77], v107 offset:17408
	s_waitcnt lgkmcnt(3)
	v_mfma_f32_16x16x32_bf16 v[42:45], v[90:93], v[86:89], v[42:45]
	v_cvt_pk_bf16_f32 v58, v58, v59
	v_cvt_pk_bf16_f32 v59, v60, v61
	ds_write_b64 v101, v[58:59] offset:768
	v_mfma_f32_16x16x32_bf16 v[6:9], v[90:93], v[120:123], v[6:9]
	ds_read_b64_tr_b16 v[82:83], v108 offset:16384
	ds_read_b64_tr_b16 v[84:85], v108 offset:17408
	s_waitcnt lgkmcnt(3)
	v_mfma_f32_16x16x32_bf16 v[58:61], v[74:77], v[86:89], v[116:119]
	v_cndmask_b32_e64 v90, 0, v169, s[10:11]
	s_mov_b32 s78, m0
	s_mov_b32 m0, s67
	s_nop 0
	global_load_lds_dwordx4 v90, s[50:51]
	s_mov_b32 m0, s78
	v_mfma_f32_16x16x32_bf16 v[112:115], v[74:77], v[120:123], v[112:115]
	s_waitcnt lgkmcnt(0)
	v_mfma_f32_16x16x32_bf16 v[116:119], v[82:85], v[86:89], v[54:57]
	s_nop 2
	ds_read_b64_tr_b16 v[54:55], v109 offset:16384
	ds_read_b64_tr_b16 v[56:57], v109 offset:17408
	v_cndmask_b32_e64 v74, 0, v170, s[10:11]
	s_mov_b32 s78, m0
	s_mov_b32 m0, s68
	s_nop 0
	global_load_lds_dwordx4 v74, s[50:51]
	s_mov_b32 m0, s78
	v_mfma_f32_16x16x32_bf16 v[34:37], v[82:85], v[120:123], v[34:37]
	ds_read_b64_tr_b16 v[74:75], v110 offset:16384
	ds_read_b64_tr_b16 v[76:77], v110 offset:17408
	s_waitcnt lgkmcnt(2)
	v_mfma_f32_16x16x32_bf16 v[30:33], v[54:57], v[86:89], v[30:33]
	v_cndmask_b32_e64 v82, 0, v174, s[10:11]
	s_mov_b32 s78, m0
	s_mov_b32 m0, s69
	s_nop 0
	global_load_lds_dwordx4 v82, s[50:51]
	s_mov_b32 m0, s78
	v_mfma_f32_16x16x32_bf16 v[14:17], v[54:57], v[120:123], v[14:17]
	ds_read_b64_tr_b16 v[54:55], v171 offset:24576
	ds_read_b64_tr_b16 v[56:57], v171 offset:25600
	ds_read_b128 v[124:127], v103
	ds_read_b128 v[136:139], v103 offset:2048
	s_waitcnt lgkmcnt(4)
	v_mfma_f32_16x16x32_bf16 v[10:13], v[74:77], v[86:89], v[10:13]
	v_cndmask_b32_e64 v82, 0, v175, s[10:11]
	s_mov_b32 s10, m0
	s_mov_b32 m0, s70
	s_nop 0
	global_load_lds_dwordx4 v82, s[50:51]
	s_mov_b32 m0, s10
	v_mfma_f32_16x16x32_bf16 v[2:5], v[74:77], v[120:123], v[2:5]
	s_waitcnt lgkmcnt(1)
	v_mfma_f32_16x16x32_bf16 v[94:97], v[54:57], v[124:127], v[46:49]
	s_nop 2
	ds_read_b64_tr_b16 v[46:47], v104 offset:24576
	ds_read_b64_tr_b16 v[48:49], v104 offset:25600
	s_waitcnt lgkmcnt(2)
	v_mfma_f32_16x16x32_bf16 v[74:77], v[54:57], v[136:139], v[62:65]
	ds_read_b64_tr_b16 v[54:55], v105 offset:24576
	ds_read_b64_tr_b16 v[56:57], v105 offset:25600
	s_waitcnt lgkmcnt(2)
	v_mfma_f32_16x16x32_bf16 v[90:93], v[46:49], v[124:127], v[78:81]
	v_mfma_f32_16x16x32_bf16 v[46:49], v[46:49], v[136:139], v[66:69]
	ds_read_b64_tr_b16 v[62:63], v106 offset:24576
	ds_read_b64_tr_b16 v[64:65], v106 offset:25600
	s_waitcnt lgkmcnt(2)
	v_mfma_f32_16x16x32_bf16 v[70:73], v[54:57], v[124:127], v[70:73]
	v_mfma_f32_16x16x32_bf16 v[18:21], v[54:57], v[136:139], v[18:21]
	ds_read_b64_tr_b16 v[54:55], v107 offset:24576
	ds_read_b64_tr_b16 v[56:57], v107 offset:25600
	s_waitcnt lgkmcnt(2)
	v_mfma_f32_16x16x32_bf16 v[42:45], v[62:65], v[124:127], v[42:45]
	v_mfma_f32_16x16x32_bf16 v[6:9], v[62:65], v[136:139], v[6:9]
	s_waitcnt lgkmcnt(0)
	v_mfma_f32_16x16x32_bf16 v[86:89], v[54:57], v[124:127], v[58:61]
	s_nop 2
	ds_read_b64_tr_b16 v[58:59], v108 offset:24576
	ds_read_b64_tr_b16 v[60:61], v108 offset:25600
	s_cbranch_vccz .Lmy_tl_878_0
	global_load_dwordx4 v[78:81], v111, s[48:49]
.Lmy_tl_878_0:
	v_mfma_f32_16x16x32_bf16 v[54:57], v[54:57], v[136:139], v[112:115]
	s_nop 2
	ds_read_b64_tr_b16 v[112:113], v109 offset:24576
	ds_read_b64_tr_b16 v[114:115], v109 offset:25600
	s_waitcnt lgkmcnt(2)
	v_mfma_f32_16x16x32_bf16 v[62:65], v[58:61], v[124:127], v[116:119]
	s_cbranch_vccz .Lmy_tl_878_1
	global_load_dwordx4 v[66:69], v111, s[48:49] offset:2048
.Lmy_tl_878_1:
	v_mfma_f32_16x16x32_bf16 v[34:37], v[58:61], v[136:139], v[34:37]
	s_nop 1
	ds_read_b64_tr_b16 v[116:117], v110 offset:24576
	ds_read_b64_tr_b16 v[118:119], v110 offset:25600
	s_waitcnt lgkmcnt(2)
	v_mfma_f32_16x16x32_bf16 v[30:33], v[112:115], v[124:127], v[30:33]
	s_add_u32 s10, s76, 0x81000
	s_addc_u32 s11, s77, 0
	s_cbranch_vccz .Lmy_tl_878_2
	global_load_dwordx4 v[82:85], v111, s[10:11]
.Lmy_tl_878_2:
	v_mfma_f32_16x16x32_bf16 v[14:17], v[112:115], v[136:139], v[14:17]
	s_waitcnt lgkmcnt(0)
	v_mfma_f32_16x16x32_bf16 v[10:13], v[116:119], v[124:127], v[10:13]
	s_cbranch_vccz .Lmy_tl_878_3
	global_load_dwordx4 v[58:61], v111, s[10:11] offset:2048
.Lmy_tl_878_3:
	v_mfma_f32_16x16x32_bf16 v[2:5], v[116:119], v[136:139], v[2:5]
	s_waitcnt lgkmcnt(0)
	s_barrier
	s_mov_b32 s50, s75
	s_cbranch_vccnz .LBB0_878
	s_waitcnt vmcnt(0)
	s_waitcnt lgkmcnt(0)
	s_barrier
	v_mov_b32_e32 v81, 0
	v_mov_b32_e32 v80, v81
	v_mov_b32_e32 v79, v81
	v_mov_b32_e32 v78, v81
	v_mov_b32_e32 v61, v81
	v_mov_b32_e32 v60, v81
	v_mov_b32_e32 v59, v81
	v_mov_b32_e32 v58, v81
	v_mov_b32_e32 v41, v81
	v_mov_b32_e32 v40, v81
	v_mov_b32_e32 v39, v81
	v_mov_b32_e32 v38, v81
	v_mov_b32_e32 v25, v81
	v_mov_b32_e32 v24, v81
	v_mov_b32_e32 v23, v81
	v_mov_b32_e32 v22, v81
	v_mov_b32_e32 v85, v81
	v_mov_b32_e32 v84, v81
	v_mov_b32_e32 v83, v81
	v_mov_b32_e32 v82, v81
	v_mov_b32_e32 v69, v81
	v_mov_b32_e32 v68, v81
	v_mov_b32_e32 v67, v81
	v_mov_b32_e32 v66, v81
	v_mov_b32_e32 v53, v81
	v_mov_b32_e32 v52, v81
	v_mov_b32_e32 v51, v81
	v_mov_b32_e32 v50, v81
	v_mov_b32_e32 v29, v81
	v_mov_b32_e32 v28, v81
	v_mov_b32_e32 v27, v81
	v_mov_b32_e32 v26, v81

.LBB0_885:
	s_waitcnt vmcnt(4)
	s_min_u32 s10, s46, 12
	ds_read_b64_tr_b16 v[196:197], v171
	ds_read_b64_tr_b16 v[198:199], v171 offset:1024
	ds_read_b128 v[200:203], v172
	ds_read_b128 v[204:207], v172 offset:2048
	ds_read_b128 v[208:211], v172 offset:4096
	ds_read_b128 v[212:215], v172 offset:6144
	s_cmp_lt_u32 s46, 13
	s_cselect_b64 vcc, -1, 0
	s_lshl_b32 s10, s10, 17
	s_add_u32 s47, s22, s10
	s_addc_u32 s80, s23, 0
	s_add_u32 s10, s47, 0x60000
	ds_read_b64_tr_b16 v[216:217], v179
	ds_read_b64_tr_b16 v[218:219], v179 offset:1024
	s_waitcnt lgkmcnt(5)
	v_mfma_f32_16x16x32_bf16 v[94:97], v[196:199], v[200:203], v[94:97]
	s_addc_u32 s11, s80, 0
	s_add_u32 s14, s8, s12
	s_addc_u32 s15, s9, s13
	s_waitcnt lgkmcnt(4)
	v_mfma_f32_16x16x32_bf16 v[74:77], v[196:199], v[204:207], v[74:77]
	s_add_u32 s14, s14, 0x80
	v_cvt_pk_bf16_f32 v138, v138, v139
	v_cvt_pk_bf16_f32 v139, v140, v141
	s_waitcnt lgkmcnt(3)
	v_mfma_f32_16x16x32_bf16 v[78:81], v[196:199], v[208:211], v[78:81]
	v_cndmask_b32_e32 v220, 0, v168, vcc
	s_addc_u32 s15, s15, 0
	ds_write_b64 v186, v[138:139] offset:16384
	s_waitcnt lgkmcnt(3)
	v_mfma_f32_16x16x32_bf16 v[122:125], v[196:199], v[212:215], v[122:125]
	ds_read_b64_tr_b16 v[138:139], v180
	ds_read_b64_tr_b16 v[140:141], v180 offset:1024
	s_waitcnt lgkmcnt(3)
	v_mfma_f32_16x16x32_bf16 v[90:93], v[216:219], v[200:203], v[90:93]
	v_cvt_pk_bf16_f32 v134, v134, v135
	v_cvt_pk_bf16_f32 v135, v136, v137
	ds_write_b64 v193, v[134:135] offset:16640
	v_mfma_f32_16x16x32_bf16 v[46:49], v[216:219], v[204:207], v[46:49]
	v_mfma_f32_16x16x32_bf16 v[58:61], v[216:219], v[208:211], v[58:61]
	v_mfma_f32_16x16x32_bf16 v[114:117], v[216:219], v[212:215], v[114:117]
	ds_read_b64_tr_b16 v[134:135], v181
	ds_read_b64_tr_b16 v[136:137], v181 offset:1024
	s_waitcnt lgkmcnt(3)
	v_mfma_f32_16x16x32_bf16 v[70:73], v[138:141], v[200:203], v[70:73]
	v_cvt_pk_bf16_f32 v142, v142, v143
	v_cvt_pk_bf16_f32 v143, v144, v145
	ds_write_b64 v194, v[142:143] offset:16896
	v_mfma_f32_16x16x32_bf16 v[18:21], v[138:141], v[204:207], v[18:21]
	v_mfma_f32_16x16x32_bf16 v[38:41], v[138:141], v[208:211], v[38:41]
	v_mfma_f32_16x16x32_bf16 v[106:109], v[138:141], v[212:215], v[106:109]
	ds_read_b64_tr_b16 v[138:139], v182
	ds_read_b64_tr_b16 v[140:141], v182 offset:1024
	s_waitcnt lgkmcnt(3)
	v_mfma_f32_16x16x32_bf16 v[42:45], v[134:137], v[200:203], v[42:45]
	v_cvt_pk_bf16_f32 v130, v130, v131
	v_cvt_pk_bf16_f32 v131, v132, v133
	ds_write_b64 v195, v[130:131] offset:17152
	v_mfma_f32_16x16x32_bf16 v[6:9], v[134:137], v[204:207], v[6:9]
	v_mfma_f32_16x16x32_bf16 v[22:25], v[134:137], v[208:211], v[22:25]
	v_mfma_f32_16x16x32_bf16 v[102:105], v[134:137], v[212:215], v[102:105]
	ds_read_b64_tr_b16 v[130:131], v183
	ds_read_b64_tr_b16 v[132:133], v183 offset:1024
	s_waitcnt lgkmcnt(3)
	v_mfma_f32_16x16x32_bf16 v[86:89], v[138:141], v[200:203], v[86:89]
	s_mov_b32 s81, m0
	s_mov_b32 m0, s71
	s_nop 0
	global_load_lds_dwordx4 v169, s[14:15]
	s_mov_b32 m0, s81
	v_mfma_f32_16x16x32_bf16 v[54:57], v[138:141], v[204:207], v[54:57]
	v_mfma_f32_16x16x32_bf16 v[82:85], v[138:141], v[208:211], v[82:85]
	v_mfma_f32_16x16x32_bf16 v[126:129], v[138:141], v[212:215], v[126:129]
	ds_read_b64_tr_b16 v[134:135], v184
	ds_read_b64_tr_b16 v[136:137], v184 offset:1024
	s_waitcnt lgkmcnt(2)
	v_mfma_f32_16x16x32_bf16 v[62:65], v[130:133], v[200:203], v[62:65]
	s_mov_b32 s81, m0
	s_mov_b32 m0, s72
	s_nop 0
	global_load_lds_dwordx4 v170, s[14:15]
	s_mov_b32 m0, s81
	v_mfma_f32_16x16x32_bf16 v[34:37], v[130:133], v[204:207], v[34:37]
	v_mfma_f32_16x16x32_bf16 v[66:69], v[130:133], v[208:211], v[66:69]
	v_mfma_f32_16x16x32_bf16 v[118:121], v[130:133], v[212:215], v[118:121]
	ds_read_b64_tr_b16 v[130:131], v185
	ds_read_b64_tr_b16 v[132:133], v185 offset:1024
	s_waitcnt lgkmcnt(2)
	v_mfma_f32_16x16x32_bf16 v[30:33], v[134:137], v[200:203], v[30:33]
	s_mov_b32 s81, m0
	s_mov_b32 m0, s73
	s_nop 0
	global_load_lds_dwordx4 v174, s[14:15]
	s_mov_b32 m0, s81
	v_mfma_f32_16x16x32_bf16 v[14:17], v[134:137], v[204:207], v[14:17]
	v_mfma_f32_16x16x32_bf16 v[50:53], v[134:137], v[208:211], v[50:53]
	v_mfma_f32_16x16x32_bf16 v[110:113], v[134:137], v[212:215], v[110:113]
	s_waitcnt lgkmcnt(0)
	v_mfma_f32_16x16x32_bf16 v[10:13], v[130:133], v[200:203], v[10:13]
	ds_read_b64_tr_b16 v[134:135], v171 offset:8192
	ds_read_b64_tr_b16 v[136:137], v171 offset:9216
	v_mfma_f32_16x16x32_bf16 v[2:5], v[130:133], v[204:207], v[2:5]
	v_mfma_f32_16x16x32_bf16 v[26:29], v[130:133], v[208:211], v[26:29]
	ds_read_b128 v[196:199], v178
	ds_read_b128 v[200:203], v178 offset:2048
	ds_read_b128 v[204:207], v178 offset:4096
	ds_read_b128 v[208:211], v178 offset:6144
	s_mov_b32 s81, m0
	s_mov_b32 m0, s74
	s_nop 0
	global_load_lds_dwordx4 v175, s[14:15]
	s_mov_b32 m0, s81
	v_mfma_f32_16x16x32_bf16 v[98:101], v[130:133], v[212:215], v[98:101]
	ds_read_b64_tr_b16 v[130:131], v179 offset:8192
	ds_read_b64_tr_b16 v[132:133], v179 offset:9216
	s_waitcnt lgkmcnt(5)
	v_mfma_f32_16x16x32_bf16 v[94:97], v[134:137], v[196:199], v[94:97]
	s_mov_b32 s81, m0
	s_mov_b32 m0, s75
	s_nop 0
	global_load_lds_dwordx4 v176, s[14:15]
	s_mov_b32 m0, s81
	s_waitcnt lgkmcnt(4)
	v_mfma_f32_16x16x32_bf16 v[74:77], v[134:137], v[200:203], v[74:77]
	s_waitcnt lgkmcnt(3)
	v_mfma_f32_16x16x32_bf16 v[78:81], v[134:137], v[204:207], v[78:81]
	s_waitcnt lgkmcnt(2)
	v_mfma_f32_16x16x32_bf16 v[122:125], v[134:137], v[208:211], v[122:125]
	ds_read_b64_tr_b16 v[134:135], v180 offset:8192
	ds_read_b64_tr_b16 v[136:137], v180 offset:9216
	s_waitcnt lgkmcnt(2)
	v_mfma_f32_16x16x32_bf16 v[90:93], v[130:133], v[196:199], v[90:93]
	s_mov_b32 s81, m0
	s_mov_b32 m0, s76
	s_nop 0
	global_load_lds_dwordx4 v177, s[14:15]
	s_mov_b32 m0, s81
	v_mfma_f32_16x16x32_bf16 v[46:49], v[130:133], v[200:203], v[46:49]
	v_mfma_f32_16x16x32_bf16 v[58:61], v[130:133], v[204:207], v[58:61]
	v_mfma_f32_16x16x32_bf16 v[114:117], v[130:133], v[208:211], v[114:117]
	ds_read_b64_tr_b16 v[130:131], v181 offset:8192
	ds_read_b64_tr_b16 v[132:133], v181 offset:9216
	s_waitcnt lgkmcnt(2)
	v_mfma_f32_16x16x32_bf16 v[70:73], v[134:137], v[196:199], v[70:73]
	s_mov_b32 s81, m0
	s_mov_b32 m0, s77
	s_nop 0
	global_load_lds_dwordx4 v191, s[14:15]
	s_mov_b32 m0, s81
	v_mfma_f32_16x16x32_bf16 v[18:21], v[134:137], v[200:203], v[18:21]
	v_mfma_f32_16x16x32_bf16 v[38:41], v[134:137], v[204:207], v[38:41]
	v_mfma_f32_16x16x32_bf16 v[106:109], v[134:137], v[208:211], v[106:109]
	ds_read_b64_tr_b16 v[134:135], v182 offset:8192
	ds_read_b64_tr_b16 v[136:137], v182 offset:9216
	s_waitcnt lgkmcnt(2)
	v_mfma_f32_16x16x32_bf16 v[42:45], v[130:133], v[196:199], v[42:45]
	s_mov_b32 s81, m0
	s_mov_b32 m0, s78
	s_nop 0
	global_load_lds_dwordx4 v192, s[14:15]
	s_mov_b32 m0, s81
	v_mfma_f32_16x16x32_bf16 v[6:9], v[130:133], v[200:203], v[6:9]
	v_mfma_f32_16x16x32_bf16 v[22:25], v[130:133], v[204:207], v[22:25]
	v_mfma_f32_16x16x32_bf16 v[102:105], v[130:133], v[208:211], v[102:105]
	ds_read_b64_tr_b16 v[130:131], v183 offset:8192
	ds_read_b64_tr_b16 v[132:133], v183 offset:9216
	s_waitcnt lgkmcnt(2)
	v_mfma_f32_16x16x32_bf16 v[86:89], v[134:137], v[196:199], v[86:89]
	global_load_dwordx4 v[138:141], v220, s[10:11]
	v_mfma_f32_16x16x32_bf16 v[54:57], v[134:137], v[200:203], v[54:57]
	v_mfma_f32_16x16x32_bf16 v[82:85], v[134:137], v[204:207], v[82:85]
	v_mfma_f32_16x16x32_bf16 v[126:129], v[134:137], v[208:211], v[126:129]
	ds_read_b64_tr_b16 v[212:213], v184 offset:8192
	ds_read_b64_tr_b16 v[214:215], v184 offset:9216
	s_waitcnt lgkmcnt(2)
	v_mfma_f32_16x16x32_bf16 v[62:65], v[130:133], v[196:199], v[62:65]
	global_load_dwordx4 v[134:137], v220, s[10:11] offset:2048
	v_mfma_f32_16x16x32_bf16 v[34:37], v[130:133], v[200:203], v[34:37]
	v_mfma_f32_16x16x32_bf16 v[66:69], v[130:133], v[204:207], v[66:69]
	v_mfma_f32_16x16x32_bf16 v[118:121], v[130:133], v[208:211], v[118:121]
	ds_read_b64_tr_b16 v[216:217], v185 offset:8192
	ds_read_b64_tr_b16 v[218:219], v185 offset:9216
	s_waitcnt lgkmcnt(2)
	v_mfma_f32_16x16x32_bf16 v[30:33], v[212:215], v[196:199], v[30:33]
	s_add_u32 s10, s47, 0x61000
	s_addc_u32 s11, s80, 0
	global_load_dwordx4 v[142:145], v220, s[10:11]
	v_mfma_f32_16x16x32_bf16 v[14:17], v[212:215], v[200:203], v[14:17]
	v_mfma_f32_16x16x32_bf16 v[50:53], v[212:215], v[204:207], v[50:53]
	v_mfma_f32_16x16x32_bf16 v[110:113], v[212:215], v[208:211], v[110:113]
	s_waitcnt lgkmcnt(0)
	v_mfma_f32_16x16x32_bf16 v[10:13], v[216:219], v[196:199], v[10:13]
	global_load_dwordx4 v[130:133], v220, s[10:11] offset:2048
	v_mfma_f32_16x16x32_bf16 v[2:5], v[216:219], v[200:203], v[2:5]
	v_mfma_f32_16x16x32_bf16 v[26:29], v[216:219], v[204:207], v[26:29]
	v_mfma_f32_16x16x32_bf16 v[98:101], v[216:219], v[208:211], v[98:101]
	s_min_u32 s10, s46, 11
	s_add_i32 s80, s46, 2
	s_cmp_lt_u32 s46, 12
	s_cselect_b64 vcc, -1, 0
	s_lshl_b32 s10, s10, 17
	s_waitcnt lgkmcnt(0)
	s_barrier
	s_add_u32 s81, s22, s10
	s_waitcnt vmcnt(4)
	s_addc_u32 s82, s23, 0
	ds_read_b64_tr_b16 v[196:197], v171 offset:16384
	ds_read_b64_tr_b16 v[198:199], v171 offset:17408
	s_add_u32 s14, s81, 0x80000
	ds_read_b128 v[200:203], v172 offset:8192
	ds_read_b128 v[204:207], v172 offset:10240
	ds_read_b128 v[208:211], v172 offset:12288
	ds_read_b128 v[212:215], v172 offset:14336
	s_addc_u32 s15, s82, 0
	s_add_u32 s12, s12, 0x100
	s_addc_u32 s13, s13, 0
	s_cmp_lt_u32 s46, 14
	ds_read_b64_tr_b16 v[216:217], v179 offset:16384
	ds_read_b64_tr_b16 v[218:219], v179 offset:17408
	s_cselect_b64 s[10:11], -1, 0
	s_waitcnt lgkmcnt(5)
	v_mfma_f32_16x16x32_bf16 v[94:97], v[196:199], v[200:203], v[94:97]
	v_cndmask_b32_e32 v220, 0, v168, vcc
	s_and_b64 vcc, s[10:11], exec
	s_cselect_b32 s46, s12, 0x780
	s_waitcnt lgkmcnt(4)
	v_mfma_f32_16x16x32_bf16 v[74:77], v[196:199], v[204:207], v[74:77]
	s_add_u32 s46, s8, s46
	v_cvt_pk_bf16_f32 v154, v154, v155
	v_cvt_pk_bf16_f32 v155, v156, v157
	s_waitcnt lgkmcnt(3)
	v_mfma_f32_16x16x32_bf16 v[78:81], v[196:199], v[208:211], v[78:81]
	s_addc_u32 s47, s9, 0
	ds_write_b64 v186, v[154:155]
	s_waitcnt lgkmcnt(3)
	v_mfma_f32_16x16x32_bf16 v[122:125], v[196:199], v[212:215], v[122:125]
	ds_read_b64_tr_b16 v[154:155], v180 offset:16384
	ds_read_b64_tr_b16 v[156:157], v180 offset:17408
	s_waitcnt lgkmcnt(3)
	v_mfma_f32_16x16x32_bf16 v[90:93], v[216:219], v[200:203], v[90:93]
	v_cvt_pk_bf16_f32 v150, v150, v151
	v_cvt_pk_bf16_f32 v151, v152, v153
	ds_write_b64 v193, v[150:151] offset:256
	v_mfma_f32_16x16x32_bf16 v[46:49], v[216:219], v[204:207], v[46:49]
	v_mfma_f32_16x16x32_bf16 v[58:61], v[216:219], v[208:211], v[58:61]
	v_mfma_f32_16x16x32_bf16 v[114:117], v[216:219], v[212:215], v[114:117]
	ds_read_b64_tr_b16 v[150:151], v181 offset:16384
	ds_read_b64_tr_b16 v[152:153], v181 offset:17408
	s_waitcnt lgkmcnt(3)
	v_mfma_f32_16x16x32_bf16 v[70:73], v[154:157], v[200:203], v[70:73]
	v_cvt_pk_bf16_f32 v158, v158, v159
	v_cvt_pk_bf16_f32 v159, v160, v161
	ds_write_b64 v194, v[158:159] offset:512
	v_mfma_f32_16x16x32_bf16 v[18:21], v[154:157], v[204:207], v[18:21]
	v_mfma_f32_16x16x32_bf16 v[38:41], v[154:157], v[208:211], v[38:41]
	v_mfma_f32_16x16x32_bf16 v[106:109], v[154:157], v[212:215], v[106:109]
	ds_read_b64_tr_b16 v[154:155], v182 offset:16384
	ds_read_b64_tr_b16 v[156:157], v182 offset:17408
	s_waitcnt lgkmcnt(3)
	v_mfma_f32_16x16x32_bf16 v[42:45], v[150:153], v[200:203], v[42:45]
	v_cvt_pk_bf16_f32 v146, v146, v147
	v_cvt_pk_bf16_f32 v147, v148, v149
	ds_write_b64 v195, v[146:147] offset:768
	v_mfma_f32_16x16x32_bf16 v[6:9], v[150:153], v[204:207], v[6:9]
	v_mfma_f32_16x16x32_bf16 v[22:25], v[150:153], v[208:211], v[22:25]
	v_mfma_f32_16x16x32_bf16 v[102:105], v[150:153], v[212:215], v[102:105]
	ds_read_b64_tr_b16 v[146:147], v183 offset:16384
	ds_read_b64_tr_b16 v[148:149], v183 offset:17408
	s_waitcnt lgkmcnt(3)
	v_mfma_f32_16x16x32_bf16 v[86:89], v[154:157], v[200:203], v[86:89]
	v_cndmask_b32_e64 v150, 0, v169, s[10:11]
	s_mov_b32 s83, m0
	s_mov_b32 m0, s67
	s_nop 0
	global_load_lds_dwordx4 v150, s[46:47]
	s_mov_b32 m0, s83
	v_mfma_f32_16x16x32_bf16 v[54:57], v[154:157], v[204:207], v[54:57]
	v_mfma_f32_16x16x32_bf16 v[82:85], v[154:157], v[208:211], v[82:85]
	v_mfma_f32_16x16x32_bf16 v[126:129], v[154:157], v[212:215], v[126:129]
	ds_read_b64_tr_b16 v[150:151], v184 offset:16384
	ds_read_b64_tr_b16 v[152:153], v184 offset:17408
	s_waitcnt lgkmcnt(2)
	v_mfma_f32_16x16x32_bf16 v[62:65], v[146:149], v[200:203], v[62:65]
	v_cndmask_b32_e64 v154, 0, v170, s[10:11]
	s_mov_b32 s83, m0
	s_mov_b32 m0, s68
	s_nop 0
	global_load_lds_dwordx4 v154, s[46:47]
	s_mov_b32 m0, s83
	v_mfma_f32_16x16x32_bf16 v[34:37], v[146:149], v[204:207], v[34:37]
	v_mfma_f32_16x16x32_bf16 v[66:69], v[146:149], v[208:211], v[66:69]
	v_mfma_f32_16x16x32_bf16 v[118:121], v[146:149], v[212:215], v[118:121]
	ds_read_b64_tr_b16 v[146:147], v185 offset:16384
	ds_read_b64_tr_b16 v[148:149], v185 offset:17408
	s_waitcnt lgkmcnt(2)
	v_mfma_f32_16x16x32_bf16 v[30:33], v[150:153], v[200:203], v[30:33]
	v_cndmask_b32_e64 v154, 0, v174, s[10:11]
	s_mov_b32 s83, m0
	s_mov_b32 m0, s48
	s_nop 0
	global_load_lds_dwordx4 v154, s[46:47]
	s_mov_b32 m0, s83
	v_mfma_f32_16x16x32_bf16 v[14:17], v[150:153], v[204:207], v[14:17]
	v_mfma_f32_16x16x32_bf16 v[50:53], v[150:153], v[208:211], v[50:53]
	v_mfma_f32_16x16x32_bf16 v[110:113], v[150:153], v[212:215], v[110:113]
	s_waitcnt lgkmcnt(0)
	v_mfma_f32_16x16x32_bf16 v[10:13], v[146:149], v[200:203], v[10:13]
	ds_read_b64_tr_b16 v[150:151], v171 offset:24576
	ds_read_b64_tr_b16 v[152:153], v171 offset:25600
	ds_read_b128 v[196:199], v187
	ds_read_b128 v[200:203], v187 offset:2048
	v_cndmask_b32_e64 v154, 0, v175, s[10:11]
	v_mfma_f32_16x16x32_bf16 v[2:5], v[146:149], v[204:207], v[2:5]
	v_mfma_f32_16x16x32_bf16 v[26:29], v[146:149], v[208:211], v[26:29]
	ds_read_b128 v[204:207], v187 offset:4096
	ds_read_b128 v[208:211], v187 offset:6144
	s_mov_b32 s83, m0
	s_mov_b32 m0, s49
	s_nop 0
	global_load_lds_dwordx4 v154, s[46:47]
	s_mov_b32 m0, s83
	v_mfma_f32_16x16x32_bf16 v[98:101], v[146:149], v[212:215], v[98:101]
	ds_read_b64_tr_b16 v[146:147], v179 offset:24576
	ds_read_b64_tr_b16 v[148:149], v179 offset:25600
	s_waitcnt lgkmcnt(5)
	v_mfma_f32_16x16x32_bf16 v[94:97], v[150:153], v[196:199], v[94:97]
	v_cndmask_b32_e64 v154, 0, v176, s[10:11]
	s_mov_b32 s83, m0
	s_mov_b32 m0, s50
	s_nop 0
	global_load_lds_dwordx4 v154, s[46:47]
	s_mov_b32 m0, s83
	s_waitcnt lgkmcnt(4)
	v_mfma_f32_16x16x32_bf16 v[74:77], v[150:153], v[200:203], v[74:77]
	s_waitcnt lgkmcnt(3)
	v_mfma_f32_16x16x32_bf16 v[78:81], v[150:153], v[204:207], v[78:81]
	s_waitcnt lgkmcnt(2)
	v_mfma_f32_16x16x32_bf16 v[122:125], v[150:153], v[208:211], v[122:125]
	ds_read_b64_tr_b16 v[150:151], v180 offset:24576
	ds_read_b64_tr_b16 v[152:153], v180 offset:25600
	s_waitcnt lgkmcnt(2)
	v_mfma_f32_16x16x32_bf16 v[90:93], v[146:149], v[196:199], v[90:93]
	v_cndmask_b32_e64 v154, 0, v177, s[10:11]
	s_mov_b32 s83, m0
	s_mov_b32 m0, s51
	s_nop 0
	global_load_lds_dwordx4 v154, s[46:47]
	s_mov_b32 m0, s83
	v_mfma_f32_16x16x32_bf16 v[46:49], v[146:149], v[200:203], v[46:49]
	v_mfma_f32_16x16x32_bf16 v[58:61], v[146:149], v[204:207], v[58:61]
	v_mfma_f32_16x16x32_bf16 v[114:117], v[146:149], v[208:211], v[114:117]
	ds_read_b64_tr_b16 v[146:147], v181 offset:24576
	ds_read_b64_tr_b16 v[148:149], v181 offset:25600
	s_waitcnt lgkmcnt(2)
	v_mfma_f32_16x16x32_bf16 v[70:73], v[150:153], v[196:199], v[70:73]
	v_cndmask_b32_e64 v154, 0, v191, s[10:11]
	s_mov_b32 s83, m0
	s_mov_b32 m0, s69
	s_nop 0
	global_load_lds_dwordx4 v154, s[46:47]
	s_mov_b32 m0, s83
	v_mfma_f32_16x16x32_bf16 v[18:21], v[150:153], v[200:203], v[18:21]
	v_mfma_f32_16x16x32_bf16 v[38:41], v[150:153], v[204:207], v[38:41]
	v_mfma_f32_16x16x32_bf16 v[106:109], v[150:153], v[208:211], v[106:109]
	ds_read_b64_tr_b16 v[150:151], v182 offset:24576
	ds_read_b64_tr_b16 v[152:153], v182 offset:25600
	s_waitcnt lgkmcnt(2)
	v_mfma_f32_16x16x32_bf16 v[42:45], v[146:149], v[196:199], v[42:45]
	v_cndmask_b32_e64 v154, 0, v192, s[10:11]
	s_mov_b32 s10, m0
	s_mov_b32 m0, s70
	s_nop 0
	global_load_lds_dwordx4 v154, s[46:47]
	s_mov_b32 m0, s10
	v_mfma_f32_16x16x32_bf16 v[6:9], v[146:149], v[200:203], v[6:9]
	v_mfma_f32_16x16x32_bf16 v[22:25], v[146:149], v[204:207], v[22:25]
	v_mfma_f32_16x16x32_bf16 v[102:105], v[146:149], v[208:211], v[102:105]
	ds_read_b64_tr_b16 v[146:147], v183 offset:24576
	ds_read_b64_tr_b16 v[148:149], v183 offset:25600
	s_waitcnt lgkmcnt(2)
	v_mfma_f32_16x16x32_bf16 v[86:89], v[150:153], v[196:199], v[86:89]
	s_cbranch_vccz .Lmy_tl_885_0
	global_load_dwordx4 v[154:157], v220, s[14:15]
.Lmy_tl_885_0:
	v_mfma_f32_16x16x32_bf16 v[54:57], v[150:153], v[200:203], v[54:57]
	v_mfma_f32_16x16x32_bf16 v[82:85], v[150:153], v[204:207], v[82:85]
	v_mfma_f32_16x16x32_bf16 v[126:129], v[150:153], v[208:211], v[126:129]
	ds_read_b64_tr_b16 v[212:213], v184 offset:24576
	ds_read_b64_tr_b16 v[214:215], v184 offset:25600
	s_waitcnt lgkmcnt(2)
	v_mfma_f32_16x16x32_bf16 v[62:65], v[146:149], v[196:199], v[62:65]
	s_cbranch_vccz .Lmy_tl_885_1
	global_load_dwordx4 v[150:153], v220, s[14:15] offset:2048
.Lmy_tl_885_1:
	v_mfma_f32_16x16x32_bf16 v[34:37], v[146:149], v[200:203], v[34:37]
	v_mfma_f32_16x16x32_bf16 v[66:69], v[146:149], v[204:207], v[66:69]
	v_mfma_f32_16x16x32_bf16 v[118:121], v[146:149], v[208:211], v[118:121]
	ds_read_b64_tr_b16 v[216:217], v185 offset:24576
	ds_read_b64_tr_b16 v[218:219], v185 offset:25600
	s_waitcnt lgkmcnt(2)
	v_mfma_f32_16x16x32_bf16 v[30:33], v[212:215], v[196:199], v[30:33]
	s_add_u32 s10, s81, 0x81000
	s_addc_u32 s11, s82, 0
	s_cbranch_vccz .Lmy_tl_885_2
	global_load_dwordx4 v[158:161], v220, s[10:11]
.Lmy_tl_885_2:
	v_mfma_f32_16x16x32_bf16 v[14:17], v[212:215], v[200:203], v[14:17]
	v_mfma_f32_16x16x32_bf16 v[50:53], v[212:215], v[204:207], v[50:53]
	v_mfma_f32_16x16x32_bf16 v[110:113], v[212:215], v[208:211], v[110:113]
	s_waitcnt lgkmcnt(0)
	v_mfma_f32_16x16x32_bf16 v[10:13], v[216:219], v[196:199], v[10:13]
	s_cbranch_vccz .Lmy_tl_885_3
	global_load_dwordx4 v[146:149], v220, s[10:11] offset:2048
.Lmy_tl_885_3:
	v_mfma_f32_16x16x32_bf16 v[2:5], v[216:219], v[200:203], v[2:5]
	v_mfma_f32_16x16x32_bf16 v[26:29], v[216:219], v[204:207], v[26:29]
	v_mfma_f32_16x16x32_bf16 v[98:101], v[216:219], v[208:211], v[98:101]
	s_waitcnt lgkmcnt(0)
	s_barrier
	s_mov_b32 s46, s80
	s_cbranch_vccnz .LBB0_885
	s_waitcnt vmcnt(0)
	s_waitcnt lgkmcnt(0)
	s_barrier
	s_mov_b64 s[12:13], 0

.LBB0_889:
	s_cmp_lt_u32 s48, 13
	s_cselect_b64 vcc, -1, 0
	s_min_u32 s10, s48, 12
	s_lshl_b32 s10, s10, 17
	s_add_u32 s49, s22, s10
	s_waitcnt vmcnt(4)
	s_addc_u32 s50, s23, 0
	ds_read_b128 v[50:53], v172
	ds_read_b64_tr_b16 v[54:55], v171
	ds_read_b64_tr_b16 v[56:57], v171 offset:1024
	s_add_u32 s10, s49, 0x60000
	ds_read_b64_tr_b16 v[58:59], v179
	ds_read_b64_tr_b16 v[60:61], v179 offset:1024
	s_addc_u32 s11, s50, 0
	s_add_u32 s14, s8, s12
	s_addc_u32 s15, s9, s13
	s_add_u32 s14, s14, 0x80
	v_cvt_pk_bf16_f32 v18, v18, v19
	v_cvt_pk_bf16_f32 v19, v20, v21
	v_cndmask_b32_e32 v49, 0, v168, vcc
	s_addc_u32 s15, s15, 0
	s_waitcnt lgkmcnt(2)
	v_mfma_f32_16x16x32_bf16 v[54:57], v[54:57], v[50:53], v[94:97]
	ds_write_b64 v186, v[18:19] offset:16384
	ds_read_b64_tr_b16 v[18:19], v180
	ds_read_b64_tr_b16 v[20:21], v180 offset:1024
	v_cvt_pk_bf16_f32 v6, v6, v7
	v_cvt_pk_bf16_f32 v7, v8, v9
	s_waitcnt lgkmcnt(3)
	v_mfma_f32_16x16x32_bf16 v[58:61], v[58:61], v[50:53], v[90:93]
	ds_write_b64 v46, v[6:7] offset:16640
	ds_read_b64_tr_b16 v[6:7], v181
	ds_read_b64_tr_b16 v[8:9], v181 offset:1024
	s_waitcnt lgkmcnt(3)
	v_mfma_f32_16x16x32_bf16 v[18:21], v[18:21], v[50:53], v[70:73]
	v_cvt_pk_bf16_f32 v14, v14, v15
	v_cvt_pk_bf16_f32 v15, v16, v17
	ds_write_b64 v47, v[14:15] offset:16896
	ds_read_b64_tr_b16 v[14:15], v182
	ds_read_b64_tr_b16 v[16:17], v182 offset:1024
	s_waitcnt lgkmcnt(3)
	v_mfma_f32_16x16x32_bf16 v[6:9], v[6:9], v[50:53], v[42:45]
	v_cvt_pk_bf16_f32 v2, v2, v3
	v_cvt_pk_bf16_f32 v3, v4, v5
	ds_write_b64 v48, v[2:3] offset:17152
	ds_read_b64_tr_b16 v[2:3], v183
	ds_read_b64_tr_b16 v[4:5], v183 offset:1024
	s_waitcnt lgkmcnt(3)
	v_mfma_f32_16x16x32_bf16 v[14:17], v[14:17], v[50:53], v[86:89]
	s_mov_b32 s51, m0
	s_mov_b32 m0, s46
	s_nop 0
	global_load_lds_dwordx4 v169, s[14:15]
	s_mov_b32 m0, s51
	ds_read_b64_tr_b16 v[42:43], v184
	ds_read_b64_tr_b16 v[44:45], v184 offset:1024
	s_waitcnt lgkmcnt(2)
	v_mfma_f32_16x16x32_bf16 v[2:5], v[2:5], v[50:53], v[62:65]
	s_mov_b32 s51, m0
	s_mov_b32 m0, s47
	s_nop 0
	global_load_lds_dwordx4 v170, s[14:15]
	s_mov_b32 m0, s51
	s_nop 2
	ds_read_b64_tr_b16 v[62:63], v185
	ds_read_b64_tr_b16 v[64:65], v185 offset:1024
	s_waitcnt lgkmcnt(2)
	v_mfma_f32_16x16x32_bf16 v[30:33], v[42:45], v[50:53], v[30:33]
	ds_read_b64_tr_b16 v[42:43], v171 offset:8192
	ds_read_b64_tr_b16 v[44:45], v171 offset:9216
	ds_read_b128 v[66:69], v178
	s_waitcnt lgkmcnt(3)
	v_mfma_f32_16x16x32_bf16 v[10:13], v[62:65], v[50:53], v[10:13]
	ds_read_b64_tr_b16 v[50:51], v179 offset:8192
	ds_read_b64_tr_b16 v[52:53], v179 offset:9216
	s_waitcnt lgkmcnt(2)
	v_mfma_f32_16x16x32_bf16 v[42:45], v[42:45], v[66:69], v[54:57]
	s_nop 2
	ds_read_b64_tr_b16 v[54:55], v180 offset:8192
	ds_read_b64_tr_b16 v[56:57], v180 offset:9216
	s_waitcnt lgkmcnt(2)
	v_mfma_f32_16x16x32_bf16 v[50:53], v[50:53], v[66:69], v[58:61]
	s_nop 2
	ds_read_b64_tr_b16 v[58:59], v181 offset:8192
	ds_read_b64_tr_b16 v[60:61], v181 offset:9216
	s_waitcnt lgkmcnt(2)
	v_mfma_f32_16x16x32_bf16 v[54:57], v[54:57], v[66:69], v[18:21]
	s_nop 2
	ds_read_b64_tr_b16 v[18:19], v182 offset:8192
	ds_read_b64_tr_b16 v[20:21], v182 offset:9216
	s_waitcnt lgkmcnt(2)
	v_mfma_f32_16x16x32_bf16 v[58:61], v[58:61], v[66:69], v[6:9]
	s_nop 2
	ds_read_b64_tr_b16 v[6:7], v183 offset:8192
	ds_read_b64_tr_b16 v[8:9], v183 offset:9216
	s_waitcnt lgkmcnt(2)
	v_mfma_f32_16x16x32_bf16 v[62:65], v[18:21], v[66:69], v[14:17]
	global_load_dwordx4 v[18:21], v49, s[10:11]
	s_nop 2
	ds_read_b64_tr_b16 v[14:15], v184 offset:8192
	ds_read_b64_tr_b16 v[16:17], v184 offset:9216
	s_waitcnt lgkmcnt(2)
	v_mfma_f32_16x16x32_bf16 v[70:73], v[6:9], v[66:69], v[2:5]
	global_load_dwordx4 v[6:9], v49, s[10:11] offset:2048
	ds_read_b64_tr_b16 v[74:75], v185 offset:8192
	ds_read_b64_tr_b16 v[76:77], v185 offset:9216
	s_waitcnt lgkmcnt(2)
	v_mfma_f32_16x16x32_bf16 v[30:33], v[14:17], v[66:69], v[30:33]
	s_add_u32 s10, s49, 0x61000
	s_addc_u32 s11, s50, 0
	global_load_dwordx4 v[14:17], v49, s[10:11]
	s_waitcnt lgkmcnt(0)
	v_mfma_f32_16x16x32_bf16 v[10:13], v[74:77], v[66:69], v[10:13]
	global_load_dwordx4 v[2:5], v49, s[10:11] offset:2048
	s_add_i32 s49, s48, 2
	s_cmp_lt_u32 s48, 12
	s_cselect_b64 vcc, -1, 0
	s_min_u32 s10, s48, 11
	s_lshl_b32 s10, s10, 17
	s_waitcnt lgkmcnt(0)
	s_barrier
	s_add_u32 s69, s22, s10
	s_waitcnt vmcnt(4)
	s_addc_u32 s70, s23, 0
	s_add_u32 s14, s69, 0x80000
	ds_read_b64_tr_b16 v[66:67], v171 offset:16384
	ds_read_b64_tr_b16 v[68:69], v171 offset:17408
	ds_read_b128 v[74:77], v172 offset:8192
	s_addc_u32 s15, s70, 0
	s_add_u32 s12, s12, 0x100
	s_addc_u32 s13, s13, 0
	s_cmp_lt_u32 s48, 14
	ds_read_b64_tr_b16 v[78:79], v179 offset:16384
	ds_read_b64_tr_b16 v[80:81], v179 offset:17408
	s_cselect_b64 s[10:11], -1, 0
	s_waitcnt lgkmcnt(2)
	v_mfma_f32_16x16x32_bf16 v[42:45], v[66:69], v[74:77], v[42:45]
	v_cndmask_b32_e32 v49, 0, v168, vcc
	s_and_b64 vcc, s[10:11], exec
	s_cselect_b32 s48, s12, 0x780
	s_add_u32 s50, s8, s48
	v_cvt_pk_bf16_f32 v38, v38, v39
	v_cvt_pk_bf16_f32 v39, v40, v41
	s_addc_u32 s51, s9, 0
	ds_write_b64 v186, v[38:39]
	ds_read_b64_tr_b16 v[38:39], v180 offset:16384
	ds_read_b64_tr_b16 v[40:41], v180 offset:17408
	v_cvt_pk_bf16_f32 v26, v26, v27
	v_cvt_pk_bf16_f32 v27, v28, v29
	s_waitcnt lgkmcnt(3)
	v_mfma_f32_16x16x32_bf16 v[50:53], v[78:81], v[74:77], v[50:53]
	ds_write_b64 v46, v[26:27] offset:256
	ds_read_b64_tr_b16 v[26:27], v181 offset:16384
	ds_read_b64_tr_b16 v[28:29], v181 offset:17408
	s_waitcnt lgkmcnt(3)
	v_mfma_f32_16x16x32_bf16 v[38:41], v[38:41], v[74:77], v[54:57]
	v_cvt_pk_bf16_f32 v34, v34, v35
	v_cvt_pk_bf16_f32 v35, v36, v37
	ds_write_b64 v47, v[34:35] offset:512
	ds_read_b64_tr_b16 v[34:35], v182 offset:16384
	ds_read_b64_tr_b16 v[36:37], v182 offset:17408
	s_waitcnt lgkmcnt(3)
	v_mfma_f32_16x16x32_bf16 v[26:29], v[26:29], v[74:77], v[58:61]
	v_cvt_pk_bf16_f32 v22, v22, v23
	v_cvt_pk_bf16_f32 v23, v24, v25
	ds_write_b64 v48, v[22:23] offset:768
	ds_read_b64_tr_b16 v[22:23], v183 offset:16384
	ds_read_b64_tr_b16 v[24:25], v183 offset:17408
	s_waitcnt lgkmcnt(3)
	v_mfma_f32_16x16x32_bf16 v[34:37], v[34:37], v[74:77], v[62:65]
	v_cndmask_b32_e64 v54, 0, v169, s[10:11]
	s_mov_b32 s48, m0
	s_mov_b32 m0, s67
	s_nop 0
	global_load_lds_dwordx4 v54, s[50:51]
	s_mov_b32 m0, s48
	ds_read_b64_tr_b16 v[54:55], v184 offset:16384
	ds_read_b64_tr_b16 v[56:57], v184 offset:17408
	s_waitcnt lgkmcnt(2)
	v_mfma_f32_16x16x32_bf16 v[22:25], v[22:25], v[74:77], v[70:73]
	v_cndmask_b32_e64 v58, 0, v170, s[10:11]
	s_mov_b32 s10, m0
	s_mov_b32 m0, s68
	s_nop 0
	global_load_lds_dwordx4 v58, s[50:51]
	s_mov_b32 m0, s10
	ds_read_b64_tr_b16 v[58:59], v185 offset:16384
	ds_read_b64_tr_b16 v[60:61], v185 offset:17408
	s_waitcnt lgkmcnt(2)
	v_mfma_f32_16x16x32_bf16 v[30:33], v[54:57], v[74:77], v[30:33]
	ds_read_b64_tr_b16 v[54:55], v171 offset:24576
	ds_read_b64_tr_b16 v[56:57], v171 offset:25600
	ds_read_b128 v[66:69], v187
	s_waitcnt lgkmcnt(3)
	v_mfma_f32_16x16x32_bf16 v[10:13], v[58:61], v[74:77], v[10:13]
	ds_read_b64_tr_b16 v[58:59], v179 offset:24576
	ds_read_b64_tr_b16 v[60:61], v179 offset:25600
	s_waitcnt lgkmcnt(2)
	v_mfma_f32_16x16x32_bf16 v[94:97], v[54:57], v[66:69], v[42:45]
	s_nop 2
	ds_read_b64_tr_b16 v[42:43], v180 offset:24576
	ds_read_b64_tr_b16 v[44:45], v180 offset:25600
	s_waitcnt lgkmcnt(2)
	v_mfma_f32_16x16x32_bf16 v[90:93], v[58:61], v[66:69], v[50:53]
	s_nop 2
	ds_read_b64_tr_b16 v[50:51], v181 offset:24576
	ds_read_b64_tr_b16 v[52:53], v181 offset:25600
	s_waitcnt lgkmcnt(2)
	v_mfma_f32_16x16x32_bf16 v[70:73], v[42:45], v[66:69], v[38:41]
	s_nop 2
	ds_read_b64_tr_b16 v[38:39], v182 offset:24576
	ds_read_b64_tr_b16 v[40:41], v182 offset:25600
	s_waitcnt lgkmcnt(2)
	v_mfma_f32_16x16x32_bf16 v[42:45], v[50:53], v[66:69], v[26:29]
	s_nop 2
	ds_read_b64_tr_b16 v[26:27], v183 offset:24576
	ds_read_b64_tr_b16 v[28:29], v183 offset:25600
	s_waitcnt lgkmcnt(2)
	v_mfma_f32_16x16x32_bf16 v[86:89], v[38:41], v[66:69], v[34:37]
	s_cbranch_vccz .Lmy_tl_889_0
	global_load_dwordx4 v[38:41], v49, s[14:15]
.Lmy_tl_889_0:
	s_nop 2
	ds_read_b64_tr_b16 v[34:35], v184 offset:24576
	ds_read_b64_tr_b16 v[36:37], v184 offset:25600
	s_waitcnt lgkmcnt(2)
	v_mfma_f32_16x16x32_bf16 v[62:65], v[26:29], v[66:69], v[22:25]
	s_cbranch_vccz .Lmy_tl_889_1
	global_load_dwordx4 v[26:29], v49, s[14:15] offset:2048
.Lmy_tl_889_1:
	ds_read_b64_tr_b16 v[50:51], v185 offset:24576
	ds_read_b64_tr_b16 v[52:53], v185 offset:25600
	s_waitcnt lgkmcnt(2)
	v_mfma_f32_16x16x32_bf16 v[30:33], v[34:37], v[66:69], v[30:33]
	s_add_u32 s10, s69, 0x81000
	s_addc_u32 s11, s70, 0
	s_cbranch_vccz .Lmy_tl_889_2
	global_load_dwordx4 v[34:37], v49, s[10:11]
.Lmy_tl_889_2:
	s_waitcnt lgkmcnt(0)
	v_mfma_f32_16x16x32_bf16 v[10:13], v[50:53], v[66:69], v[10:13]
	s_cbranch_vccz .Lmy_tl_889_3
	global_load_dwordx4 v[22:25], v49, s[10:11] offset:2048
.Lmy_tl_889_3:
	s_waitcnt lgkmcnt(0)
	s_barrier
	s_mov_b32 s48, s49
	s_cbranch_vccnz .LBB0_889
	s_waitcnt vmcnt(0)
	s_waitcnt lgkmcnt(0)
	s_barrier
	v_mov_b32_e32 v77, 0
	v_mov_b32_e32 v76, v77
	v_mov_b32_e32 v75, v77
	v_mov_b32_e32 v74, v77
	v_mov_b32_e32 v81, v77
	v_mov_b32_e32 v80, v77
	v_mov_b32_e32 v79, v77
	v_mov_b32_e32 v78, v77
	v_mov_b32_e32 v125, v77
	v_mov_b32_e32 v124, v77
	v_mov_b32_e32 v123, v77
	v_mov_b32_e32 v122, v77
	v_mov_b32_e32 v49, v77
	v_mov_b32_e32 v48, v77
	v_mov_b32_e32 v47, v77
	v_mov_b32_e32 v46, v77
	v_mov_b32_e32 v61, v77
	v_mov_b32_e32 v60, v77
	v_mov_b32_e32 v59, v77
	v_mov_b32_e32 v58, v77
	v_mov_b32_e32 v117, v77
	v_mov_b32_e32 v116, v77
	v_mov_b32_e32 v115, v77
	v_mov_b32_e32 v114, v77
	v_mov_b32_e32 v21, v77
	v_mov_b32_e32 v20, v77
	v_mov_b32_e32 v19, v77
	v_mov_b32_e32 v18, v77
	v_mov_b32_e32 v41, v77
	v_mov_b32_e32 v40, v77
	v_mov_b32_e32 v39, v77
	v_mov_b32_e32 v38, v77
	v_mov_b32_e32 v109, v77
	v_mov_b32_e32 v108, v77
	v_mov_b32_e32 v107, v77
	v_mov_b32_e32 v106, v77
	v_mov_b32_e32 v9, v77
	v_mov_b32_e32 v8, v77
	v_mov_b32_e32 v7, v77
	v_mov_b32_e32 v6, v77
	v_mov_b32_e32 v25, v77
	v_mov_b32_e32 v24, v77
	v_mov_b32_e32 v23, v77
	v_mov_b32_e32 v22, v77
	v_mov_b32_e32 v105, v77
	v_mov_b32_e32 v104, v77
	v_mov_b32_e32 v103, v77
	v_mov_b32_e32 v102, v77
	v_mov_b32_e32 v57, v77
	v_mov_b32_e32 v56, v77
	v_mov_b32_e32 v55, v77
	v_mov_b32_e32 v54, v77
	v_mov_b32_e32 v85, v77
	v_mov_b32_e32 v84, v77
	v_mov_b32_e32 v83, v77
	v_mov_b32_e32 v82, v77
	v_mov_b32_e32 v129, v77
	v_mov_b32_e32 v128, v77
	v_mov_b32_e32 v127, v77
	v_mov_b32_e32 v126, v77
	v_mov_b32_e32 v37, v77
	v_mov_b32_e32 v36, v77
	v_mov_b32_e32 v35, v77
	v_mov_b32_e32 v34, v77
	v_mov_b32_e32 v69, v77
	v_mov_b32_e32 v68, v77
	v_mov_b32_e32 v67, v77
	v_mov_b32_e32 v66, v77
	v_mov_b32_e32 v121, v77
	v_mov_b32_e32 v120, v77
	v_mov_b32_e32 v119, v77
	v_mov_b32_e32 v118, v77
	v_mov_b32_e32 v17, v77
	v_mov_b32_e32 v16, v77
	v_mov_b32_e32 v15, v77
	v_mov_b32_e32 v14, v77
	v_mov_b32_e32 v53, v77
	v_mov_b32_e32 v52, v77
	v_mov_b32_e32 v51, v77
	v_mov_b32_e32 v50, v77
	v_mov_b32_e32 v113, v77
	v_mov_b32_e32 v112, v77
	v_mov_b32_e32 v111, v77
	v_mov_b32_e32 v110, v77
	v_mov_b32_e32 v5, v77
	v_mov_b32_e32 v4, v77
	v_mov_b32_e32 v3, v77
	v_mov_b32_e32 v2, v77
	v_mov_b32_e32 v29, v77
	v_mov_b32_e32 v28, v77
	v_mov_b32_e32 v27, v77
	v_mov_b32_e32 v26, v77
	v_mov_b32_e32 v101, v77
	v_mov_b32_e32 v100, v77
	v_mov_b32_e32 v99, v77
	v_mov_b32_e32 v98, v77
